# gate fast log-sigmoid + GEMM K-loops: all 16 staging loads per loop body in scalar-base form (b3/a3 parked in spare scalar pairs), no VALU left in the load segments
# baseline (speedup 1.0000x reference)
.LBB0_119:
	ds_read_b128 v[148:151], v153
	ds_read_b128 v[156:159], v153 offset:1024
	ds_read_b128 v[160:163], v153 offset:2048
	ds_read_b128 v[164:167], v153 offset:3072
	ds_read_b128 v[168:171], v154
	ds_read_b128 v[172:175], v154 offset:1024
	ds_read_b128 v[176:179], v154 offset:2048
	ds_read_b128 v[180:183], v154 offset:3072
	s_add_u32 s24, s22, 0xfff80080
	s_addc_u32 s25, s23, -1
	s_cmp_eq_u32 s79, 28
	s_cselect_b32 s27, s15, s25
	s_cselect_b32 s26, s75, s24
	s_cselect_b32 s25, s13, s78
	s_cselect_b32 s24, s76, s77
	s_add_i32 m0, s21, 0xc000
	ds_read_b128 v[184:187], v155
	ds_read_b128 v[188:191], v155 offset:1024
	ds_read_b128 v[192:195], v155 offset:2048
	ds_read_b128 v[196:199], v155 offset:3072
	ds_read_b128 v[200:203], v155 offset:4096
	ds_read_b128 v[204:207], v155 offset:5120
	ds_read_b128 v[208:211], v155 offset:6144
	ds_read_b128 v[212:215], v155 offset:7168
	global_load_lds_dwordx4 v140, s[22:23]
	s_add_i32 m0, s21, 0xe000
	s_nop 0
	global_load_lds_dwordx4 v142, s[22:23]
	s_waitcnt vmcnt(8)
	s_waitcnt lgkmcnt(0)
	s_barrier
	s_setprio 1
	s_waitcnt lgkmcnt(0)
	v_mfma_f32_16x16x32_bf16 v[126:129], v[148:151], v[184:187], v[126:129]
	v_mfma_f32_16x16x32_bf16 v[122:125], v[160:163], v[184:187], v[122:125]
	v_mfma_f32_16x16x32_bf16 v[118:121], v[148:151], v[192:195], v[118:121]
	v_mfma_f32_16x16x32_bf16 v[110:113], v[160:163], v[192:195], v[110:113]
	v_mfma_f32_16x16x32_bf16 v[102:105], v[148:151], v[200:203], v[102:105]
	v_mfma_f32_16x16x32_bf16 v[94:97], v[160:163], v[200:203], v[94:97]
	v_mfma_f32_16x16x32_bf16 v[86:89], v[148:151], v[208:211], v[86:89]
	v_mfma_f32_16x16x32_bf16 v[78:81], v[160:163], v[208:211], v[78:81]
	v_mfma_f32_16x16x32_bf16 v[126:129], v[156:159], v[188:191], v[126:129]
	v_mfma_f32_16x16x32_bf16 v[122:125], v[164:167], v[188:191], v[122:125]
	v_mfma_f32_16x16x32_bf16 v[118:121], v[156:159], v[196:199], v[118:121]
	v_mfma_f32_16x16x32_bf16 v[110:113], v[164:167], v[196:199], v[110:113]
	v_mfma_f32_16x16x32_bf16 v[102:105], v[156:159], v[204:207], v[102:105]
	v_mfma_f32_16x16x32_bf16 v[94:97], v[164:167], v[204:207], v[94:97]
	v_mfma_f32_16x16x32_bf16 v[86:89], v[156:159], v[212:215], v[86:89]
	v_mfma_f32_16x16x32_bf16 v[78:81], v[164:167], v[212:215], v[78:81]
	s_setprio 0
	s_setprio 1
	v_mfma_f32_16x16x32_bf16 v[114:117], v[168:171], v[184:187], v[114:117]
	v_mfma_f32_16x16x32_bf16 v[106:109], v[176:179], v[184:187], v[106:109]
	v_mfma_f32_16x16x32_bf16 v[98:101], v[168:171], v[192:195], v[98:101]
	v_mfma_f32_16x16x32_bf16 v[90:93], v[176:179], v[192:195], v[90:93]
	v_mfma_f32_16x16x32_bf16 v[82:85], v[168:171], v[200:203], v[82:85]
	v_mfma_f32_16x16x32_bf16 v[74:77], v[176:179], v[200:203], v[74:77]
	v_mfma_f32_16x16x32_bf16 v[70:73], v[168:171], v[208:211], v[70:73]
	v_mfma_f32_16x16x32_bf16 v[66:69], v[176:179], v[208:211], v[66:69]
	v_mfma_f32_16x16x32_bf16 v[114:117], v[172:175], v[188:191], v[114:117]
	v_mfma_f32_16x16x32_bf16 v[106:109], v[180:183], v[188:191], v[106:109]
	v_mfma_f32_16x16x32_bf16 v[98:101], v[172:175], v[196:199], v[98:101]
	v_mfma_f32_16x16x32_bf16 v[90:93], v[180:183], v[196:199], v[90:93]
	v_mfma_f32_16x16x32_bf16 v[82:85], v[172:175], v[204:207], v[82:85]
	v_mfma_f32_16x16x32_bf16 v[74:77], v[180:183], v[204:207], v[74:77]
	v_mfma_f32_16x16x32_bf16 v[70:73], v[172:175], v[212:215], v[70:73]
	v_mfma_f32_16x16x32_bf16 v[66:69], v[180:183], v[212:215], v[66:69]
	s_setprio 0
	s_barrier
	s_add_i32 s80, s71, s33
	s_mov_b32 m0, s80
	ds_read_b128 v[184:187], v155 offset:16384
	ds_read_b128 v[188:191], v155 offset:17408
	ds_read_b128 v[192:195], v155 offset:18432
	ds_read_b128 v[196:199], v155 offset:19456
	ds_read_b128 v[200:203], v155 offset:20480
	ds_read_b128 v[204:207], v155 offset:21504
	ds_read_b128 v[208:211], v155 offset:22528
	ds_read_b128 v[212:215], v155 offset:23552
	global_load_lds_dwordx4 v136, s[24:25]
	s_add_i32 m0, s80, 0x2000
	s_add_u32 s80, s24, 0x80000
	s_addc_u32 s81, s25, 0
	s_add_i32 s82, s72, s33
	global_load_lds_dwordx4 v132, s[24:25]
	s_mov_b32 m0, s82
	s_nop 0
	global_load_lds_dwordx4 v136, s[80:81]
	s_add_i32 m0, s82, 0x2000
	s_nop 0
	global_load_lds_dwordx4 v132, s[80:81]
	s_mov_b32 m0, s21
	s_nop 0
	global_load_lds_dwordx4 v138, s[26:27]
	s_mov_b32 m0, s36
	s_nop 0
	global_load_lds_dwordx4 v134, s[26:27]
	s_add_u32 s98, s24, 0x80
	s_addc_u32 s99, s25, 0
	s_add_u32 s100, s26, 0x80
	s_addc_u32 s101, s27, 0
	s_waitcnt vmcnt(8)
	s_waitcnt lgkmcnt(0)
	s_barrier
	s_setprio 1
	s_waitcnt lgkmcnt(0)
	v_mfma_f32_16x16x32_bf16 v[62:65], v[148:151], v[184:187], v[62:65]
	v_mfma_f32_16x16x32_bf16 v[58:61], v[160:163], v[184:187], v[58:61]
	v_mfma_f32_16x16x32_bf16 v[54:57], v[148:151], v[192:195], v[54:57]
	v_mfma_f32_16x16x32_bf16 v[46:49], v[160:163], v[192:195], v[46:49]
	v_mfma_f32_16x16x32_bf16 v[38:41], v[148:151], v[200:203], v[38:41]
	v_mfma_f32_16x16x32_bf16 v[30:33], v[160:163], v[200:203], v[30:33]
	v_mfma_f32_16x16x32_bf16 v[22:25], v[148:151], v[208:211], v[22:25]
	v_mfma_f32_16x16x32_bf16 v[14:17], v[160:163], v[208:211], v[14:17]
	v_mfma_f32_16x16x32_bf16 v[62:65], v[156:159], v[188:191], v[62:65]
	v_mfma_f32_16x16x32_bf16 v[58:61], v[164:167], v[188:191], v[58:61]
	v_mfma_f32_16x16x32_bf16 v[54:57], v[156:159], v[196:199], v[54:57]
	v_mfma_f32_16x16x32_bf16 v[46:49], v[164:167], v[196:199], v[46:49]
	v_mfma_f32_16x16x32_bf16 v[38:41], v[156:159], v[204:207], v[38:41]
	v_mfma_f32_16x16x32_bf16 v[30:33], v[164:167], v[204:207], v[30:33]
	v_mfma_f32_16x16x32_bf16 v[22:25], v[156:159], v[212:215], v[22:25]
	v_mfma_f32_16x16x32_bf16 v[14:17], v[164:167], v[212:215], v[14:17]
	s_setprio 0
	s_setprio 1
	v_mfma_f32_16x16x32_bf16 v[50:53], v[168:171], v[184:187], v[50:53]
	v_mfma_f32_16x16x32_bf16 v[42:45], v[176:179], v[184:187], v[42:45]
	v_mfma_f32_16x16x32_bf16 v[34:37], v[168:171], v[192:195], v[34:37]
	v_mfma_f32_16x16x32_bf16 v[26:29], v[176:179], v[192:195], v[26:29]
	v_mfma_f32_16x16x32_bf16 v[18:21], v[168:171], v[200:203], v[18:21]
	v_mfma_f32_16x16x32_bf16 v[10:13], v[176:179], v[200:203], v[10:13]
	v_mfma_f32_16x16x32_bf16 v[6:9], v[168:171], v[208:211], v[6:9]
	v_mfma_f32_16x16x32_bf16 v[2:5], v[176:179], v[208:211], v[2:5]
	v_mfma_f32_16x16x32_bf16 v[50:53], v[172:175], v[188:191], v[50:53]
	v_mfma_f32_16x16x32_bf16 v[42:45], v[180:183], v[188:191], v[42:45]
	v_mfma_f32_16x16x32_bf16 v[34:37], v[172:175], v[196:199], v[34:37]
	v_mfma_f32_16x16x32_bf16 v[26:29], v[180:183], v[196:199], v[26:29]
	v_mfma_f32_16x16x32_bf16 v[18:21], v[172:175], v[204:207], v[18:21]
	v_mfma_f32_16x16x32_bf16 v[10:13], v[180:183], v[204:207], v[10:13]
	v_mfma_f32_16x16x32_bf16 v[6:9], v[172:175], v[212:215], v[6:9]
	v_mfma_f32_16x16x32_bf16 v[2:5], v[180:183], v[212:215], v[2:5]
	s_setprio 0
	s_barrier
	s_add_i32 s80, 0, 0x18000
	s_add_i32 s81, 0, 0x1c000
	v_add_u32_e32 v164, s80, v131
	v_add_u32_e32 v180, s81, v131
	ds_read_b128 v[148:151], v164
	ds_read_b128 v[156:159], v164 offset:1024
	ds_read_b128 v[160:163], v164 offset:2048
	ds_read_b128 v[164:167], v164 offset:3072
	ds_read_b128 v[168:171], v180
	ds_read_b128 v[172:175], v180 offset:1024
	ds_read_b128 v[176:179], v180 offset:2048
	ds_read_b128 v[180:183], v180 offset:3072
	s_add_u32 s26, s26, 0x80000
	s_addc_u32 s27, s27, 0
	s_mov_b32 m0, s37
	ds_read_b128 v[184:187], v155 offset:32768
	ds_read_b128 v[188:191], v155 offset:33792
	ds_read_b128 v[192:195], v155 offset:34816
	ds_read_b128 v[196:199], v155 offset:35840
	ds_read_b128 v[200:203], v155 offset:36864
	ds_read_b128 v[204:207], v155 offset:37888
	ds_read_b128 v[208:211], v155 offset:38912
	ds_read_b128 v[212:215], v155 offset:39936
	global_load_lds_dwordx4 v138, s[26:27]
	s_mov_b32 m0, s42
	s_nop 0
	global_load_lds_dwordx4 v134, s[26:27]
	s_waitcnt vmcnt(8)
	s_waitcnt lgkmcnt(0)
	s_barrier
	s_setprio 1
	s_waitcnt lgkmcnt(0)
	v_mfma_f32_16x16x32_bf16 v[126:129], v[148:151], v[184:187], v[126:129]
	v_mfma_f32_16x16x32_bf16 v[122:125], v[160:163], v[184:187], v[122:125]
	v_mfma_f32_16x16x32_bf16 v[118:121], v[148:151], v[192:195], v[118:121]
	v_mfma_f32_16x16x32_bf16 v[110:113], v[160:163], v[192:195], v[110:113]
	v_mfma_f32_16x16x32_bf16 v[102:105], v[148:151], v[200:203], v[102:105]
	v_mfma_f32_16x16x32_bf16 v[94:97], v[160:163], v[200:203], v[94:97]
	v_mfma_f32_16x16x32_bf16 v[86:89], v[148:151], v[208:211], v[86:89]
	v_mfma_f32_16x16x32_bf16 v[78:81], v[160:163], v[208:211], v[78:81]
	v_mfma_f32_16x16x32_bf16 v[126:129], v[156:159], v[188:191], v[126:129]
	v_mfma_f32_16x16x32_bf16 v[122:125], v[164:167], v[188:191], v[122:125]
	v_mfma_f32_16x16x32_bf16 v[118:121], v[156:159], v[196:199], v[118:121]
	v_mfma_f32_16x16x32_bf16 v[110:113], v[164:167], v[196:199], v[110:113]
	v_mfma_f32_16x16x32_bf16 v[102:105], v[156:159], v[204:207], v[102:105]
	v_mfma_f32_16x16x32_bf16 v[94:97], v[164:167], v[204:207], v[94:97]
	v_mfma_f32_16x16x32_bf16 v[86:89], v[156:159], v[212:215], v[86:89]
	v_mfma_f32_16x16x32_bf16 v[78:81], v[164:167], v[212:215], v[78:81]
	s_setprio 0
	s_setprio 1
	v_mfma_f32_16x16x32_bf16 v[114:117], v[168:171], v[184:187], v[114:117]
	v_mfma_f32_16x16x32_bf16 v[106:109], v[176:179], v[184:187], v[106:109]
	v_mfma_f32_16x16x32_bf16 v[98:101], v[168:171], v[192:195], v[98:101]
	v_mfma_f32_16x16x32_bf16 v[90:93], v[176:179], v[192:195], v[90:93]
	v_mfma_f32_16x16x32_bf16 v[82:85], v[168:171], v[200:203], v[82:85]
	v_mfma_f32_16x16x32_bf16 v[74:77], v[176:179], v[200:203], v[74:77]
	v_mfma_f32_16x16x32_bf16 v[70:73], v[168:171], v[208:211], v[70:73]
	v_mfma_f32_16x16x32_bf16 v[66:69], v[176:179], v[208:211], v[66:69]
	v_mfma_f32_16x16x32_bf16 v[114:117], v[172:175], v[188:191], v[114:117]
	v_mfma_f32_16x16x32_bf16 v[106:109], v[180:183], v[188:191], v[106:109]
	v_mfma_f32_16x16x32_bf16 v[98:101], v[172:175], v[196:199], v[98:101]
	v_mfma_f32_16x16x32_bf16 v[90:93], v[180:183], v[196:199], v[90:93]
	v_mfma_f32_16x16x32_bf16 v[82:85], v[172:175], v[204:207], v[82:85]
	v_mfma_f32_16x16x32_bf16 v[74:77], v[180:183], v[204:207], v[74:77]
	v_mfma_f32_16x16x32_bf16 v[70:73], v[172:175], v[212:215], v[70:73]
	v_mfma_f32_16x16x32_bf16 v[66:69], v[180:183], v[212:215], v[66:69]
	s_setprio 0
	s_barrier
	s_add_i32 s26, s80, s33
	s_mov_b32 m0, s26
	ds_read_b128 v[184:187], v155 offset:49152
	ds_read_b128 v[188:191], v155 offset:50176
	ds_read_b128 v[192:195], v155 offset:51200
	ds_read_b128 v[196:199], v155 offset:52224
	ds_read_b128 v[200:203], v155 offset:53248
	ds_read_b128 v[204:207], v155 offset:54272
	ds_read_b128 v[208:211], v155 offset:55296
	ds_read_b128 v[212:215], v155 offset:56320
	global_load_lds_dwordx4 v136, s[98:99]
	s_add_i32 m0, s26, 0x2000
	s_add_u32 s24, s24, 0x80080
	s_addc_u32 s25, s25, 0
	s_add_i32 s26, s81, s33
	global_load_lds_dwordx4 v132, s[98:99]
	s_mov_b32 m0, s26
	s_nop 0
	global_load_lds_dwordx4 v136, s[24:25]
	s_add_i32 m0, s26, 0x2000
	s_nop 0
	global_load_lds_dwordx4 v132, s[24:25]
	s_mov_b32 m0, s44
	s_nop 0
	global_load_lds_dwordx4 v138, s[100:101]
	s_mov_b32 m0, s45
	s_nop 0
	global_load_lds_dwordx4 v134, s[100:101]
	s_waitcnt vmcnt(8)
	s_waitcnt lgkmcnt(0)
	s_barrier
	s_setprio 1
	s_waitcnt lgkmcnt(0)
	v_mfma_f32_16x16x32_bf16 v[62:65], v[148:151], v[184:187], v[62:65]
	v_mfma_f32_16x16x32_bf16 v[58:61], v[160:163], v[184:187], v[58:61]
	v_mfma_f32_16x16x32_bf16 v[54:57], v[148:151], v[192:195], v[54:57]
	v_mfma_f32_16x16x32_bf16 v[46:49], v[160:163], v[192:195], v[46:49]
	v_mfma_f32_16x16x32_bf16 v[38:41], v[148:151], v[200:203], v[38:41]
	v_mfma_f32_16x16x32_bf16 v[30:33], v[160:163], v[200:203], v[30:33]
	v_mfma_f32_16x16x32_bf16 v[22:25], v[148:151], v[208:211], v[22:25]
	v_mfma_f32_16x16x32_bf16 v[14:17], v[160:163], v[208:211], v[14:17]
	v_mfma_f32_16x16x32_bf16 v[62:65], v[156:159], v[188:191], v[62:65]
	v_mfma_f32_16x16x32_bf16 v[58:61], v[164:167], v[188:191], v[58:61]
	v_mfma_f32_16x16x32_bf16 v[54:57], v[156:159], v[196:199], v[54:57]
	v_mfma_f32_16x16x32_bf16 v[46:49], v[164:167], v[196:199], v[46:49]
	v_mfma_f32_16x16x32_bf16 v[38:41], v[156:159], v[204:207], v[38:41]
	v_mfma_f32_16x16x32_bf16 v[30:33], v[164:167], v[204:207], v[30:33]
	v_mfma_f32_16x16x32_bf16 v[22:25], v[156:159], v[212:215], v[22:25]
	v_mfma_f32_16x16x32_bf16 v[14:17], v[164:167], v[212:215], v[14:17]
	s_setprio 0
	s_setprio 1
	v_mfma_f32_16x16x32_bf16 v[50:53], v[168:171], v[184:187], v[50:53]
	v_mfma_f32_16x16x32_bf16 v[42:45], v[176:179], v[184:187], v[42:45]
	v_mfma_f32_16x16x32_bf16 v[34:37], v[168:171], v[192:195], v[34:37]
	v_mfma_f32_16x16x32_bf16 v[26:29], v[176:179], v[192:195], v[26:29]
	v_mfma_f32_16x16x32_bf16 v[18:21], v[168:171], v[200:203], v[18:21]
	v_mfma_f32_16x16x32_bf16 v[10:13], v[176:179], v[200:203], v[10:13]
	v_mfma_f32_16x16x32_bf16 v[6:9], v[168:171], v[208:211], v[6:9]
	v_mfma_f32_16x16x32_bf16 v[2:5], v[176:179], v[208:211], v[2:5]
	v_mfma_f32_16x16x32_bf16 v[50:53], v[172:175], v[188:191], v[50:53]
	v_mfma_f32_16x16x32_bf16 v[42:45], v[180:183], v[188:191], v[42:45]
	v_mfma_f32_16x16x32_bf16 v[34:37], v[172:175], v[196:199], v[34:37]
	v_mfma_f32_16x16x32_bf16 v[26:29], v[180:183], v[196:199], v[26:29]
	v_mfma_f32_16x16x32_bf16 v[18:21], v[172:175], v[204:207], v[18:21]
	v_mfma_f32_16x16x32_bf16 v[10:13], v[180:183], v[204:207], v[10:13]
	v_mfma_f32_16x16x32_bf16 v[6:9], v[172:175], v[212:215], v[6:9]
	v_mfma_f32_16x16x32_bf16 v[2:5], v[180:183], v[212:215], v[2:5]
	s_setprio 0
	s_barrier
	s_add_i32 s79, s79, 2
	s_add_u32 s22, s22, 0x100
	s_addc_u32 s23, s23, 0
	s_add_u32 s77, s77, 0x100
	s_addc_u32 s78, s78, 0
	s_cmp_gt_u32 s79, 29
	s_cbranch_scc0 .LBB0_119
	s_and_b64 vcc, exec, s[10:11]
	s_cbranch_vccz .LBB0_122
	s_barrier

.LBB0_466:
	ds_read_b128 v[150:153], v211
	ds_read_b128 v[154:157], v211 offset:1024
	ds_read_b128 v[158:161], v211 offset:2048
	ds_read_b128 v[162:165], v211 offset:3072
	ds_read_b128 v[166:169], v212
	ds_read_b128 v[170:173], v212 offset:1024
	ds_read_b128 v[174:177], v212 offset:2048
	ds_read_b128 v[178:181], v212 offset:3072
	s_add_u32 s42, s36, 0xfff80080
	s_addc_u32 s43, s37, -1
	s_cmp_eq_u32 s83, 28
	s_cselect_b32 s45, s1, s43
	s_cselect_b32 s44, s27, s42
	s_cselect_b32 s43, s25, s63
	s_cselect_b32 s42, s35, s62
	s_add_i32 m0, s67, 0xc000
	ds_read_b128 v[182:185], v213
	ds_read_b128 v[186:189], v213 offset:1024
	ds_read_b128 v[190:193], v213 offset:2048
	ds_read_b128 v[194:197], v213 offset:3072
	ds_read_b128 v[198:201], v213 offset:4096
	ds_read_b128 v[202:205], v213 offset:5120
	ds_read_b128 v[218:221], v213 offset:6144
	ds_read_b128 v[222:225], v213 offset:7168
	global_load_lds_dwordx4 v142, s[36:37]
	s_add_i32 m0, s67, 0xe000
	s_nop 0
	global_load_lds_dwordx4 v144, s[36:37]
	s_waitcnt vmcnt(8)
	s_waitcnt lgkmcnt(0)
	s_barrier
	s_setprio 1
	s_waitcnt lgkmcnt(0)
	v_mfma_f32_16x16x32_bf16 v[126:129], v[150:153], v[182:185], v[126:129]
	v_mfma_f32_16x16x32_bf16 v[122:125], v[158:161], v[182:185], v[122:125]
	v_mfma_f32_16x16x32_bf16 v[110:113], v[150:153], v[190:193], v[110:113]
	v_mfma_f32_16x16x32_bf16 v[106:109], v[158:161], v[190:193], v[106:109]
	v_mfma_f32_16x16x32_bf16 v[94:97], v[150:153], v[198:201], v[94:97]
	v_mfma_f32_16x16x32_bf16 v[90:93], v[158:161], v[198:201], v[90:93]
	v_mfma_f32_16x16x32_bf16 v[78:81], v[150:153], v[218:221], v[78:81]
	v_mfma_f32_16x16x32_bf16 v[74:77], v[158:161], v[218:221], v[74:77]
	v_mfma_f32_16x16x32_bf16 v[126:129], v[154:157], v[186:189], v[126:129]
	v_mfma_f32_16x16x32_bf16 v[122:125], v[162:165], v[186:189], v[122:125]
	v_mfma_f32_16x16x32_bf16 v[110:113], v[154:157], v[194:197], v[110:113]
	v_mfma_f32_16x16x32_bf16 v[106:109], v[162:165], v[194:197], v[106:109]
	v_mfma_f32_16x16x32_bf16 v[94:97], v[154:157], v[202:205], v[94:97]
	v_mfma_f32_16x16x32_bf16 v[90:93], v[162:165], v[202:205], v[90:93]
	v_mfma_f32_16x16x32_bf16 v[78:81], v[154:157], v[222:225], v[78:81]
	v_mfma_f32_16x16x32_bf16 v[74:77], v[162:165], v[222:225], v[74:77]
	s_setprio 0
	s_setprio 1
	v_mfma_f32_16x16x32_bf16 v[118:121], v[166:169], v[182:185], v[118:121]
	v_mfma_f32_16x16x32_bf16 v[114:117], v[174:177], v[182:185], v[114:117]
	v_mfma_f32_16x16x32_bf16 v[102:105], v[166:169], v[190:193], v[102:105]
	v_mfma_f32_16x16x32_bf16 v[98:101], v[174:177], v[190:193], v[98:101]
	v_mfma_f32_16x16x32_bf16 v[86:89], v[166:169], v[198:201], v[86:89]
	v_mfma_f32_16x16x32_bf16 v[82:85], v[174:177], v[198:201], v[82:85]
	v_mfma_f32_16x16x32_bf16 v[70:73], v[166:169], v[218:221], v[70:73]
	v_mfma_f32_16x16x32_bf16 v[66:69], v[174:177], v[218:221], v[66:69]
	v_mfma_f32_16x16x32_bf16 v[118:121], v[170:173], v[186:189], v[118:121]
	v_mfma_f32_16x16x32_bf16 v[114:117], v[178:181], v[186:189], v[114:117]
	v_mfma_f32_16x16x32_bf16 v[102:105], v[170:173], v[194:197], v[102:105]
	v_mfma_f32_16x16x32_bf16 v[98:101], v[178:181], v[194:197], v[98:101]
	v_mfma_f32_16x16x32_bf16 v[86:89], v[170:173], v[202:205], v[86:89]
	v_mfma_f32_16x16x32_bf16 v[82:85], v[178:181], v[202:205], v[82:85]
	v_mfma_f32_16x16x32_bf16 v[70:73], v[170:173], v[222:225], v[70:73]
	v_mfma_f32_16x16x32_bf16 v[66:69], v[178:181], v[222:225], v[66:69]
	s_setprio 0
	s_barrier
	s_add_i32 s84, s79, s66
	s_mov_b32 m0, s84
	ds_read_b128 v[182:185], v213 offset:16384
	ds_read_b128 v[186:189], v213 offset:17408
	ds_read_b128 v[190:193], v213 offset:18432
	ds_read_b128 v[194:197], v213 offset:19456
	ds_read_b128 v[198:201], v213 offset:20480
	ds_read_b128 v[202:205], v213 offset:21504
	ds_read_b128 v[218:221], v213 offset:22528
	ds_read_b128 v[222:225], v213 offset:23552
	global_load_lds_dwordx4 v132, s[42:43]
	s_add_i32 m0, s84, 0x2000
	s_add_u32 s84, s42, 0x80000
	s_addc_u32 s85, s43, 0
	s_add_i32 s86, s80, s66
	global_load_lds_dwordx4 v136, s[42:43]
	s_mov_b32 m0, s86
	s_nop 0
	global_load_lds_dwordx4 v132, s[84:85]
	s_add_i32 m0, s86, 0x2000
	s_nop 0
	global_load_lds_dwordx4 v136, s[84:85]
	s_mov_b32 m0, s67
	s_nop 0
	global_load_lds_dwordx4 v130, s[44:45]
	s_mov_b32 m0, s68
	s_nop 0
	global_load_lds_dwordx4 v134, s[44:45]
	s_add_u32 s98, s42, 0x80
	s_addc_u32 s99, s43, 0
	s_add_u32 s100, s44, 0x80
	s_addc_u32 s101, s45, 0
	s_waitcnt vmcnt(8)
	s_waitcnt lgkmcnt(0)
	s_barrier
	s_setprio 1
	s_waitcnt lgkmcnt(0)
	v_mfma_f32_16x16x32_bf16 v[62:65], v[150:153], v[182:185], v[62:65]
	v_mfma_f32_16x16x32_bf16 v[58:61], v[158:161], v[182:185], v[58:61]
	v_mfma_f32_16x16x32_bf16 v[46:49], v[150:153], v[190:193], v[46:49]
	v_mfma_f32_16x16x32_bf16 v[42:45], v[158:161], v[190:193], v[42:45]
	v_mfma_f32_16x16x32_bf16 v[30:33], v[150:153], v[198:201], v[30:33]
	v_mfma_f32_16x16x32_bf16 v[26:29], v[158:161], v[198:201], v[26:29]
	v_mfma_f32_16x16x32_bf16 v[14:17], v[150:153], v[218:221], v[14:17]
	v_mfma_f32_16x16x32_bf16 v[10:13], v[158:161], v[218:221], v[10:13]
	v_mfma_f32_16x16x32_bf16 v[62:65], v[154:157], v[186:189], v[62:65]
	v_mfma_f32_16x16x32_bf16 v[58:61], v[162:165], v[186:189], v[58:61]
	v_mfma_f32_16x16x32_bf16 v[46:49], v[154:157], v[194:197], v[46:49]
	v_mfma_f32_16x16x32_bf16 v[42:45], v[162:165], v[194:197], v[42:45]
	v_mfma_f32_16x16x32_bf16 v[30:33], v[154:157], v[202:205], v[30:33]
	v_mfma_f32_16x16x32_bf16 v[26:29], v[162:165], v[202:205], v[26:29]
	v_mfma_f32_16x16x32_bf16 v[14:17], v[154:157], v[222:225], v[14:17]
	v_mfma_f32_16x16x32_bf16 v[10:13], v[162:165], v[222:225], v[10:13]
	s_setprio 0
	s_setprio 1
	v_mfma_f32_16x16x32_bf16 v[54:57], v[166:169], v[182:185], v[54:57]
	v_mfma_f32_16x16x32_bf16 v[50:53], v[174:177], v[182:185], v[50:53]
	v_mfma_f32_16x16x32_bf16 v[38:41], v[166:169], v[190:193], v[38:41]
	v_mfma_f32_16x16x32_bf16 v[34:37], v[174:177], v[190:193], v[34:37]
	v_mfma_f32_16x16x32_bf16 v[22:25], v[166:169], v[198:201], v[22:25]
	v_mfma_f32_16x16x32_bf16 v[18:21], v[174:177], v[198:201], v[18:21]
	v_mfma_f32_16x16x32_bf16 v[6:9], v[166:169], v[218:221], v[6:9]
	v_mfma_f32_16x16x32_bf16 v[2:5], v[174:177], v[218:221], v[2:5]
	v_mfma_f32_16x16x32_bf16 v[54:57], v[170:173], v[186:189], v[54:57]
	v_mfma_f32_16x16x32_bf16 v[50:53], v[178:181], v[186:189], v[50:53]
	v_mfma_f32_16x16x32_bf16 v[38:41], v[170:173], v[194:197], v[38:41]
	v_mfma_f32_16x16x32_bf16 v[34:37], v[178:181], v[194:197], v[34:37]
	v_mfma_f32_16x16x32_bf16 v[22:25], v[170:173], v[202:205], v[22:25]
	v_mfma_f32_16x16x32_bf16 v[18:21], v[178:181], v[202:205], v[18:21]
	v_mfma_f32_16x16x32_bf16 v[6:9], v[170:173], v[222:225], v[6:9]
	v_mfma_f32_16x16x32_bf16 v[2:5], v[178:181], v[222:225], v[2:5]
	s_setprio 0
	s_barrier
	s_add_i32 s84, 0, 0x18000
	v_add_u32_e32 v139, s84, v206
	s_add_i32 s85, 0, 0x1c000
	ds_read_b128 v[150:153], v139
	ds_read_b128 v[154:157], v139 offset:1024
	ds_read_b128 v[158:161], v139 offset:2048
	ds_read_b128 v[162:165], v139 offset:3072
	v_add_u32_e32 v139, s85, v206
	ds_read_b128 v[166:169], v139
	ds_read_b128 v[170:173], v139 offset:1024
	ds_read_b128 v[174:177], v139 offset:2048
	ds_read_b128 v[178:181], v139 offset:3072
	s_add_u32 s44, s44, 0x80000
	s_addc_u32 s45, s45, 0
	s_mov_b32 m0, s69
	ds_read_b128 v[182:185], v213 offset:32768
	ds_read_b128 v[186:189], v213 offset:33792
	ds_read_b128 v[190:193], v213 offset:34816
	ds_read_b128 v[194:197], v213 offset:35840
	ds_read_b128 v[198:201], v213 offset:36864
	ds_read_b128 v[202:205], v213 offset:37888
	ds_read_b128 v[218:221], v213 offset:38912
	ds_read_b128 v[222:225], v213 offset:39936
	global_load_lds_dwordx4 v130, s[44:45]
	s_mov_b32 m0, s70
	s_nop 0
	global_load_lds_dwordx4 v134, s[44:45]
	s_waitcnt vmcnt(8)
	s_waitcnt lgkmcnt(0)
	s_barrier
	s_setprio 1
	s_waitcnt lgkmcnt(0)
	v_mfma_f32_16x16x32_bf16 v[126:129], v[150:153], v[182:185], v[126:129]
	v_mfma_f32_16x16x32_bf16 v[122:125], v[158:161], v[182:185], v[122:125]
	v_mfma_f32_16x16x32_bf16 v[110:113], v[150:153], v[190:193], v[110:113]
	v_mfma_f32_16x16x32_bf16 v[106:109], v[158:161], v[190:193], v[106:109]
	v_mfma_f32_16x16x32_bf16 v[94:97], v[150:153], v[198:201], v[94:97]
	v_mfma_f32_16x16x32_bf16 v[90:93], v[158:161], v[198:201], v[90:93]
	v_mfma_f32_16x16x32_bf16 v[78:81], v[150:153], v[218:221], v[78:81]
	v_mfma_f32_16x16x32_bf16 v[74:77], v[158:161], v[218:221], v[74:77]
	v_mfma_f32_16x16x32_bf16 v[126:129], v[154:157], v[186:189], v[126:129]
	v_mfma_f32_16x16x32_bf16 v[122:125], v[162:165], v[186:189], v[122:125]
	v_mfma_f32_16x16x32_bf16 v[110:113], v[154:157], v[194:197], v[110:113]
	v_mfma_f32_16x16x32_bf16 v[106:109], v[162:165], v[194:197], v[106:109]
	v_mfma_f32_16x16x32_bf16 v[94:97], v[154:157], v[202:205], v[94:97]
	v_mfma_f32_16x16x32_bf16 v[90:93], v[162:165], v[202:205], v[90:93]
	v_mfma_f32_16x16x32_bf16 v[78:81], v[154:157], v[222:225], v[78:81]
	v_mfma_f32_16x16x32_bf16 v[74:77], v[162:165], v[222:225], v[74:77]
	s_setprio 0
	s_setprio 1
	v_mfma_f32_16x16x32_bf16 v[118:121], v[166:169], v[182:185], v[118:121]
	v_mfma_f32_16x16x32_bf16 v[114:117], v[174:177], v[182:185], v[114:117]
	v_mfma_f32_16x16x32_bf16 v[102:105], v[166:169], v[190:193], v[102:105]
	v_mfma_f32_16x16x32_bf16 v[98:101], v[174:177], v[190:193], v[98:101]
	v_mfma_f32_16x16x32_bf16 v[86:89], v[166:169], v[198:201], v[86:89]
	v_mfma_f32_16x16x32_bf16 v[82:85], v[174:177], v[198:201], v[82:85]
	v_mfma_f32_16x16x32_bf16 v[70:73], v[166:169], v[218:221], v[70:73]
	v_mfma_f32_16x16x32_bf16 v[66:69], v[174:177], v[218:221], v[66:69]
	v_mfma_f32_16x16x32_bf16 v[118:121], v[170:173], v[186:189], v[118:121]
	v_mfma_f32_16x16x32_bf16 v[114:117], v[178:181], v[186:189], v[114:117]
	v_mfma_f32_16x16x32_bf16 v[102:105], v[170:173], v[194:197], v[102:105]
	v_mfma_f32_16x16x32_bf16 v[98:101], v[178:181], v[194:197], v[98:101]
	v_mfma_f32_16x16x32_bf16 v[86:89], v[170:173], v[202:205], v[86:89]
	v_mfma_f32_16x16x32_bf16 v[82:85], v[178:181], v[202:205], v[82:85]
	v_mfma_f32_16x16x32_bf16 v[70:73], v[170:173], v[222:225], v[70:73]
	v_mfma_f32_16x16x32_bf16 v[66:69], v[178:181], v[222:225], v[66:69]
	s_setprio 0
	s_barrier
	s_add_i32 s44, s84, s66
	s_mov_b32 m0, s44
	ds_read_b128 v[182:185], v213 offset:49152
	ds_read_b128 v[186:189], v213 offset:50176
	ds_read_b128 v[190:193], v213 offset:51200
	ds_read_b128 v[194:197], v213 offset:52224
	ds_read_b128 v[198:201], v213 offset:53248
	ds_read_b128 v[202:205], v213 offset:54272
	ds_read_b128 v[218:221], v213 offset:55296
	ds_read_b128 v[222:225], v213 offset:56320
	global_load_lds_dwordx4 v132, s[98:99]
	s_add_i32 m0, s44, 0x2000
	s_add_u32 s42, s42, 0x80080
	s_addc_u32 s43, s43, 0
	s_add_i32 s44, s85, s66
	global_load_lds_dwordx4 v136, s[98:99]
	s_mov_b32 m0, s44
	s_nop 0
	global_load_lds_dwordx4 v132, s[42:43]
	s_add_i32 m0, s44, 0x2000
	s_nop 0
	global_load_lds_dwordx4 v136, s[42:43]
	s_mov_b32 m0, s74
	s_nop 0
	global_load_lds_dwordx4 v130, s[100:101]
	s_mov_b32 m0, s75
	s_nop 0
	global_load_lds_dwordx4 v134, s[100:101]
	s_waitcnt vmcnt(8)
	s_waitcnt lgkmcnt(0)
	s_barrier
	s_setprio 1
	s_waitcnt lgkmcnt(0)
	v_mfma_f32_16x16x32_bf16 v[62:65], v[150:153], v[182:185], v[62:65]
	v_mfma_f32_16x16x32_bf16 v[58:61], v[158:161], v[182:185], v[58:61]
	v_mfma_f32_16x16x32_bf16 v[46:49], v[150:153], v[190:193], v[46:49]
	v_mfma_f32_16x16x32_bf16 v[42:45], v[158:161], v[190:193], v[42:45]
	v_mfma_f32_16x16x32_bf16 v[30:33], v[150:153], v[198:201], v[30:33]
	v_mfma_f32_16x16x32_bf16 v[26:29], v[158:161], v[198:201], v[26:29]
	v_mfma_f32_16x16x32_bf16 v[14:17], v[150:153], v[218:221], v[14:17]
	v_mfma_f32_16x16x32_bf16 v[10:13], v[158:161], v[218:221], v[10:13]
	v_mfma_f32_16x16x32_bf16 v[62:65], v[154:157], v[186:189], v[62:65]
	v_mfma_f32_16x16x32_bf16 v[58:61], v[162:165], v[186:189], v[58:61]
	v_mfma_f32_16x16x32_bf16 v[46:49], v[154:157], v[194:197], v[46:49]
	v_mfma_f32_16x16x32_bf16 v[42:45], v[162:165], v[194:197], v[42:45]
	v_mfma_f32_16x16x32_bf16 v[30:33], v[154:157], v[202:205], v[30:33]
	v_mfma_f32_16x16x32_bf16 v[26:29], v[162:165], v[202:205], v[26:29]
	v_mfma_f32_16x16x32_bf16 v[14:17], v[154:157], v[222:225], v[14:17]
	v_mfma_f32_16x16x32_bf16 v[10:13], v[162:165], v[222:225], v[10:13]
	s_setprio 0
	s_setprio 1
	v_mfma_f32_16x16x32_bf16 v[54:57], v[166:169], v[182:185], v[54:57]
	v_mfma_f32_16x16x32_bf16 v[50:53], v[174:177], v[182:185], v[50:53]
	v_mfma_f32_16x16x32_bf16 v[38:41], v[166:169], v[190:193], v[38:41]
	v_mfma_f32_16x16x32_bf16 v[34:37], v[174:177], v[190:193], v[34:37]
	v_mfma_f32_16x16x32_bf16 v[22:25], v[166:169], v[198:201], v[22:25]
	v_mfma_f32_16x16x32_bf16 v[18:21], v[174:177], v[198:201], v[18:21]
	v_mfma_f32_16x16x32_bf16 v[6:9], v[166:169], v[218:221], v[6:9]
	v_mfma_f32_16x16x32_bf16 v[2:5], v[174:177], v[218:221], v[2:5]
	v_mfma_f32_16x16x32_bf16 v[54:57], v[170:173], v[186:189], v[54:57]
	v_mfma_f32_16x16x32_bf16 v[50:53], v[178:181], v[186:189], v[50:53]
	v_mfma_f32_16x16x32_bf16 v[38:41], v[170:173], v[194:197], v[38:41]
	v_mfma_f32_16x16x32_bf16 v[34:37], v[178:181], v[194:197], v[34:37]
	v_mfma_f32_16x16x32_bf16 v[22:25], v[170:173], v[202:205], v[22:25]
	v_mfma_f32_16x16x32_bf16 v[18:21], v[178:181], v[202:205], v[18:21]
	v_mfma_f32_16x16x32_bf16 v[6:9], v[170:173], v[222:225], v[6:9]
	v_mfma_f32_16x16x32_bf16 v[2:5], v[178:181], v[222:225], v[2:5]
	s_setprio 0
	s_barrier
	s_add_i32 s83, s83, 2
	s_add_u32 s36, s36, 0x100
	s_addc_u32 s37, s37, 0
	s_add_u32 s62, s62, 0x100
	s_addc_u32 s63, s63, 0
	s_cmp_gt_u32 s83, 29
	s_cbranch_scc0 .LBB0_466
	s_and_b64 vcc, exec, s[20:21]
	s_cbranch_vccz .LBB0_469
	s_barrier

.LBB0_574:
	ds_read_b128 v[146:149], v152
	ds_read_b128 v[156:159], v152 offset:1024
	ds_read_b128 v[160:163], v152 offset:2048
	ds_read_b128 v[164:167], v152 offset:3072
	ds_read_b128 v[168:171], v153
	ds_read_b128 v[172:175], v153 offset:1024
	ds_read_b128 v[176:179], v153 offset:2048
	ds_read_b128 v[180:183], v153 offset:3072
	s_add_u32 s24, s22, 0xfff80080
	s_addc_u32 s25, s23, -1
	s_cmp_eq_u32 s69, 28
	s_cselect_b32 s27, s15, s25
	s_cselect_b32 s26, s65, s24
	s_cselect_b32 s25, s13, s68
	s_cselect_b32 s24, s66, s67
	s_add_i32 m0, s21, 0xc000
	ds_read_b128 v[184:187], v154
	ds_read_b128 v[188:191], v154 offset:1024
	ds_read_b128 v[192:195], v154 offset:2048
	ds_read_b128 v[196:199], v154 offset:3072
	ds_read_b128 v[200:203], v154 offset:4096
	ds_read_b128 v[204:207], v154 offset:5120
	ds_read_b128 v[208:211], v154 offset:6144
	ds_read_b128 v[212:215], v154 offset:7168
	global_load_lds_dwordx4 v138, s[22:23]
	s_add_i32 m0, s21, 0xe000
	s_nop 0
	global_load_lds_dwordx4 v140, s[22:23]
	s_waitcnt vmcnt(8)
	s_waitcnt lgkmcnt(0)
	s_barrier
	s_setprio 1
	s_waitcnt lgkmcnt(0)
	v_mfma_f32_16x16x32_bf16 v[126:129], v[146:149], v[184:187], v[126:129]
	v_mfma_f32_16x16x32_bf16 v[122:125], v[160:163], v[184:187], v[122:125]
	v_mfma_f32_16x16x32_bf16 v[110:113], v[146:149], v[192:195], v[110:113]
	v_mfma_f32_16x16x32_bf16 v[106:109], v[160:163], v[192:195], v[106:109]
	v_mfma_f32_16x16x32_bf16 v[94:97], v[146:149], v[200:203], v[94:97]
	v_mfma_f32_16x16x32_bf16 v[90:93], v[160:163], v[200:203], v[90:93]
	v_mfma_f32_16x16x32_bf16 v[78:81], v[146:149], v[208:211], v[78:81]
	v_mfma_f32_16x16x32_bf16 v[74:77], v[160:163], v[208:211], v[74:77]
	v_mfma_f32_16x16x32_bf16 v[126:129], v[156:159], v[188:191], v[126:129]
	v_mfma_f32_16x16x32_bf16 v[122:125], v[164:167], v[188:191], v[122:125]
	v_mfma_f32_16x16x32_bf16 v[110:113], v[156:159], v[196:199], v[110:113]
	v_mfma_f32_16x16x32_bf16 v[106:109], v[164:167], v[196:199], v[106:109]
	v_mfma_f32_16x16x32_bf16 v[94:97], v[156:159], v[204:207], v[94:97]
	v_mfma_f32_16x16x32_bf16 v[90:93], v[164:167], v[204:207], v[90:93]
	v_mfma_f32_16x16x32_bf16 v[78:81], v[156:159], v[212:215], v[78:81]
	v_mfma_f32_16x16x32_bf16 v[74:77], v[164:167], v[212:215], v[74:77]
	s_setprio 0
	s_setprio 1
	v_mfma_f32_16x16x32_bf16 v[118:121], v[168:171], v[184:187], v[118:121]
	v_mfma_f32_16x16x32_bf16 v[114:117], v[176:179], v[184:187], v[114:117]
	v_mfma_f32_16x16x32_bf16 v[102:105], v[168:171], v[192:195], v[102:105]
	v_mfma_f32_16x16x32_bf16 v[98:101], v[176:179], v[192:195], v[98:101]
	v_mfma_f32_16x16x32_bf16 v[86:89], v[168:171], v[200:203], v[86:89]
	v_mfma_f32_16x16x32_bf16 v[82:85], v[176:179], v[200:203], v[82:85]
	v_mfma_f32_16x16x32_bf16 v[70:73], v[168:171], v[208:211], v[70:73]
	v_mfma_f32_16x16x32_bf16 v[66:69], v[176:179], v[208:211], v[66:69]
	v_mfma_f32_16x16x32_bf16 v[118:121], v[172:175], v[188:191], v[118:121]
	v_mfma_f32_16x16x32_bf16 v[114:117], v[180:183], v[188:191], v[114:117]
	v_mfma_f32_16x16x32_bf16 v[102:105], v[172:175], v[196:199], v[102:105]
	v_mfma_f32_16x16x32_bf16 v[98:101], v[180:183], v[196:199], v[98:101]
	v_mfma_f32_16x16x32_bf16 v[86:89], v[172:175], v[204:207], v[86:89]
	v_mfma_f32_16x16x32_bf16 v[82:85], v[180:183], v[204:207], v[82:85]
	v_mfma_f32_16x16x32_bf16 v[70:73], v[172:175], v[212:215], v[70:73]
	v_mfma_f32_16x16x32_bf16 v[66:69], v[180:183], v[212:215], v[66:69]
	s_setprio 0
	s_barrier
	s_add_i32 s70, s61, s33
	s_mov_b32 m0, s70
	ds_read_b128 v[184:187], v154 offset:16384
	ds_read_b128 v[188:191], v154 offset:17408
	ds_read_b128 v[192:195], v154 offset:18432
	ds_read_b128 v[196:199], v154 offset:19456
	ds_read_b128 v[200:203], v154 offset:20480
	ds_read_b128 v[204:207], v154 offset:21504
	ds_read_b128 v[208:211], v154 offset:22528
	ds_read_b128 v[212:215], v154 offset:23552
	global_load_lds_dwordx4 v134, s[24:25]
	s_add_i32 m0, s70, 0x2000
	s_add_u32 s70, s24, 0x80000
	s_addc_u32 s71, s25, 0
	s_add_i32 s72, s62, s33
	global_load_lds_dwordx4 v130, s[24:25]
	s_mov_b32 m0, s72
	s_nop 0
	global_load_lds_dwordx4 v134, s[70:71]
	s_add_i32 m0, s72, 0x2000
	s_nop 0
	global_load_lds_dwordx4 v130, s[70:71]
	s_mov_b32 m0, s21
	s_nop 0
	global_load_lds_dwordx4 v136, s[26:27]
	s_mov_b32 m0, s36
	s_nop 0
	global_load_lds_dwordx4 v132, s[26:27]
	s_add_u32 s98, s24, 0x80
	s_addc_u32 s99, s25, 0
	s_add_u32 s100, s26, 0x80
	s_addc_u32 s101, s27, 0
	s_waitcnt vmcnt(8)
	s_waitcnt lgkmcnt(0)
	s_barrier
	s_setprio 1
	s_waitcnt lgkmcnt(0)
	v_mfma_f32_16x16x32_bf16 v[62:65], v[146:149], v[184:187], v[62:65]
	v_mfma_f32_16x16x32_bf16 v[58:61], v[160:163], v[184:187], v[58:61]
	v_mfma_f32_16x16x32_bf16 v[46:49], v[146:149], v[192:195], v[46:49]
	v_mfma_f32_16x16x32_bf16 v[42:45], v[160:163], v[192:195], v[42:45]
	v_mfma_f32_16x16x32_bf16 v[30:33], v[146:149], v[200:203], v[30:33]
	v_mfma_f32_16x16x32_bf16 v[26:29], v[160:163], v[200:203], v[26:29]
	v_mfma_f32_16x16x32_bf16 v[14:17], v[146:149], v[208:211], v[14:17]
	v_mfma_f32_16x16x32_bf16 v[10:13], v[160:163], v[208:211], v[10:13]
	v_mfma_f32_16x16x32_bf16 v[62:65], v[156:159], v[188:191], v[62:65]
	v_mfma_f32_16x16x32_bf16 v[58:61], v[164:167], v[188:191], v[58:61]
	v_mfma_f32_16x16x32_bf16 v[46:49], v[156:159], v[196:199], v[46:49]
	v_mfma_f32_16x16x32_bf16 v[42:45], v[164:167], v[196:199], v[42:45]
	v_mfma_f32_16x16x32_bf16 v[30:33], v[156:159], v[204:207], v[30:33]
	v_mfma_f32_16x16x32_bf16 v[26:29], v[164:167], v[204:207], v[26:29]
	v_mfma_f32_16x16x32_bf16 v[14:17], v[156:159], v[212:215], v[14:17]
	v_mfma_f32_16x16x32_bf16 v[10:13], v[164:167], v[212:215], v[10:13]
	s_setprio 0
	s_setprio 1
	v_mfma_f32_16x16x32_bf16 v[54:57], v[168:171], v[184:187], v[54:57]
	v_mfma_f32_16x16x32_bf16 v[50:53], v[176:179], v[184:187], v[50:53]
	v_mfma_f32_16x16x32_bf16 v[38:41], v[168:171], v[192:195], v[38:41]
	v_mfma_f32_16x16x32_bf16 v[34:37], v[176:179], v[192:195], v[34:37]
	v_mfma_f32_16x16x32_bf16 v[22:25], v[168:171], v[200:203], v[22:25]
	v_mfma_f32_16x16x32_bf16 v[18:21], v[176:179], v[200:203], v[18:21]
	v_mfma_f32_16x16x32_bf16 v[6:9], v[168:171], v[208:211], v[6:9]
	v_mfma_f32_16x16x32_bf16 v[2:5], v[176:179], v[208:211], v[2:5]
	v_mfma_f32_16x16x32_bf16 v[54:57], v[172:175], v[188:191], v[54:57]
	v_mfma_f32_16x16x32_bf16 v[50:53], v[180:183], v[188:191], v[50:53]
	v_mfma_f32_16x16x32_bf16 v[38:41], v[172:175], v[196:199], v[38:41]
	v_mfma_f32_16x16x32_bf16 v[34:37], v[180:183], v[196:199], v[34:37]
	v_mfma_f32_16x16x32_bf16 v[22:25], v[172:175], v[204:207], v[22:25]
	v_mfma_f32_16x16x32_bf16 v[18:21], v[180:183], v[204:207], v[18:21]
	v_mfma_f32_16x16x32_bf16 v[6:9], v[172:175], v[212:215], v[6:9]
	v_mfma_f32_16x16x32_bf16 v[2:5], v[180:183], v[212:215], v[2:5]
	s_setprio 0
	s_barrier
	s_add_i32 s70, 0, 0x18000
	v_add_u32_e32 v155, s70, v150
	s_add_i32 s71, 0, 0x1c000
	ds_read_b128 v[146:149], v155
	ds_read_b128 v[156:159], v155 offset:1024
	ds_read_b128 v[160:163], v155 offset:2048
	ds_read_b128 v[164:167], v155 offset:3072
	v_add_u32_e32 v155, s71, v150
	ds_read_b128 v[168:171], v155
	ds_read_b128 v[172:175], v155 offset:1024
	ds_read_b128 v[176:179], v155 offset:2048
	ds_read_b128 v[180:183], v155 offset:3072
	s_add_u32 s26, s26, 0x80000
	s_addc_u32 s27, s27, 0
	s_mov_b32 m0, s37
	ds_read_b128 v[184:187], v154 offset:32768
	ds_read_b128 v[188:191], v154 offset:33792
	ds_read_b128 v[192:195], v154 offset:34816
	ds_read_b128 v[196:199], v154 offset:35840
	ds_read_b128 v[200:203], v154 offset:36864
	ds_read_b128 v[204:207], v154 offset:37888
	ds_read_b128 v[208:211], v154 offset:38912
	ds_read_b128 v[212:215], v154 offset:39936
	global_load_lds_dwordx4 v136, s[26:27]
	s_mov_b32 m0, s42
	s_nop 0
	global_load_lds_dwordx4 v132, s[26:27]
	s_waitcnt vmcnt(8)
	s_waitcnt lgkmcnt(0)
	s_barrier
	s_setprio 1
	s_waitcnt lgkmcnt(0)
	v_mfma_f32_16x16x32_bf16 v[126:129], v[146:149], v[184:187], v[126:129]
	v_mfma_f32_16x16x32_bf16 v[122:125], v[160:163], v[184:187], v[122:125]
	v_mfma_f32_16x16x32_bf16 v[110:113], v[146:149], v[192:195], v[110:113]
	v_mfma_f32_16x16x32_bf16 v[106:109], v[160:163], v[192:195], v[106:109]
	v_mfma_f32_16x16x32_bf16 v[94:97], v[146:149], v[200:203], v[94:97]
	v_mfma_f32_16x16x32_bf16 v[90:93], v[160:163], v[200:203], v[90:93]
	v_mfma_f32_16x16x32_bf16 v[78:81], v[146:149], v[208:211], v[78:81]
	v_mfma_f32_16x16x32_bf16 v[74:77], v[160:163], v[208:211], v[74:77]
	v_mfma_f32_16x16x32_bf16 v[126:129], v[156:159], v[188:191], v[126:129]
	v_mfma_f32_16x16x32_bf16 v[122:125], v[164:167], v[188:191], v[122:125]
	v_mfma_f32_16x16x32_bf16 v[110:113], v[156:159], v[196:199], v[110:113]
	v_mfma_f32_16x16x32_bf16 v[106:109], v[164:167], v[196:199], v[106:109]
	v_mfma_f32_16x16x32_bf16 v[94:97], v[156:159], v[204:207], v[94:97]
	v_mfma_f32_16x16x32_bf16 v[90:93], v[164:167], v[204:207], v[90:93]
	v_mfma_f32_16x16x32_bf16 v[78:81], v[156:159], v[212:215], v[78:81]
	v_mfma_f32_16x16x32_bf16 v[74:77], v[164:167], v[212:215], v[74:77]
	s_setprio 0
	s_setprio 1
	v_mfma_f32_16x16x32_bf16 v[118:121], v[168:171], v[184:187], v[118:121]
	v_mfma_f32_16x16x32_bf16 v[114:117], v[176:179], v[184:187], v[114:117]
	v_mfma_f32_16x16x32_bf16 v[102:105], v[168:171], v[192:195], v[102:105]
	v_mfma_f32_16x16x32_bf16 v[98:101], v[176:179], v[192:195], v[98:101]
	v_mfma_f32_16x16x32_bf16 v[86:89], v[168:171], v[200:203], v[86:89]
	v_mfma_f32_16x16x32_bf16 v[82:85], v[176:179], v[200:203], v[82:85]
	v_mfma_f32_16x16x32_bf16 v[70:73], v[168:171], v[208:211], v[70:73]
	v_mfma_f32_16x16x32_bf16 v[66:69], v[176:179], v[208:211], v[66:69]
	v_mfma_f32_16x16x32_bf16 v[118:121], v[172:175], v[188:191], v[118:121]
	v_mfma_f32_16x16x32_bf16 v[114:117], v[180:183], v[188:191], v[114:117]
	v_mfma_f32_16x16x32_bf16 v[102:105], v[172:175], v[196:199], v[102:105]
	v_mfma_f32_16x16x32_bf16 v[98:101], v[180:183], v[196:199], v[98:101]
	v_mfma_f32_16x16x32_bf16 v[86:89], v[172:175], v[204:207], v[86:89]
	v_mfma_f32_16x16x32_bf16 v[82:85], v[180:183], v[204:207], v[82:85]
	v_mfma_f32_16x16x32_bf16 v[70:73], v[172:175], v[212:215], v[70:73]
	v_mfma_f32_16x16x32_bf16 v[66:69], v[180:183], v[212:215], v[66:69]
	s_setprio 0
	s_barrier
	s_add_i32 s26, s70, s33
	s_mov_b32 m0, s26
	ds_read_b128 v[184:187], v154 offset:49152
	ds_read_b128 v[188:191], v154 offset:50176
	ds_read_b128 v[192:195], v154 offset:51200
	ds_read_b128 v[196:199], v154 offset:52224
	ds_read_b128 v[200:203], v154 offset:53248
	ds_read_b128 v[204:207], v154 offset:54272
	ds_read_b128 v[208:211], v154 offset:55296
	ds_read_b128 v[212:215], v154 offset:56320
	global_load_lds_dwordx4 v134, s[98:99]
	s_add_i32 m0, s26, 0x2000
	s_add_u32 s24, s24, 0x80080
	s_addc_u32 s25, s25, 0
	s_add_i32 s26, s71, s33
	global_load_lds_dwordx4 v130, s[98:99]
	s_mov_b32 m0, s26
	s_nop 0
	global_load_lds_dwordx4 v134, s[24:25]
	s_add_i32 m0, s26, 0x2000
	s_nop 0
	global_load_lds_dwordx4 v130, s[24:25]
	s_mov_b32 m0, s44
	s_nop 0
	global_load_lds_dwordx4 v136, s[100:101]
	s_mov_b32 m0, s45
	s_nop 0
	global_load_lds_dwordx4 v132, s[100:101]
	s_waitcnt vmcnt(8)
	s_waitcnt lgkmcnt(0)
	s_barrier
	s_setprio 1
	s_waitcnt lgkmcnt(0)
	v_mfma_f32_16x16x32_bf16 v[62:65], v[146:149], v[184:187], v[62:65]
	v_mfma_f32_16x16x32_bf16 v[58:61], v[160:163], v[184:187], v[58:61]
	v_mfma_f32_16x16x32_bf16 v[46:49], v[146:149], v[192:195], v[46:49]
	v_mfma_f32_16x16x32_bf16 v[42:45], v[160:163], v[192:195], v[42:45]
	v_mfma_f32_16x16x32_bf16 v[30:33], v[146:149], v[200:203], v[30:33]
	v_mfma_f32_16x16x32_bf16 v[26:29], v[160:163], v[200:203], v[26:29]
	v_mfma_f32_16x16x32_bf16 v[14:17], v[146:149], v[208:211], v[14:17]
	v_mfma_f32_16x16x32_bf16 v[10:13], v[160:163], v[208:211], v[10:13]
	v_mfma_f32_16x16x32_bf16 v[62:65], v[156:159], v[188:191], v[62:65]
	v_mfma_f32_16x16x32_bf16 v[58:61], v[164:167], v[188:191], v[58:61]
	v_mfma_f32_16x16x32_bf16 v[46:49], v[156:159], v[196:199], v[46:49]
	v_mfma_f32_16x16x32_bf16 v[42:45], v[164:167], v[196:199], v[42:45]
	v_mfma_f32_16x16x32_bf16 v[30:33], v[156:159], v[204:207], v[30:33]
	v_mfma_f32_16x16x32_bf16 v[26:29], v[164:167], v[204:207], v[26:29]
	v_mfma_f32_16x16x32_bf16 v[14:17], v[156:159], v[212:215], v[14:17]
	v_mfma_f32_16x16x32_bf16 v[10:13], v[164:167], v[212:215], v[10:13]
	s_setprio 0
	s_setprio 1
	v_mfma_f32_16x16x32_bf16 v[54:57], v[168:171], v[184:187], v[54:57]
	v_mfma_f32_16x16x32_bf16 v[50:53], v[176:179], v[184:187], v[50:53]
	v_mfma_f32_16x16x32_bf16 v[38:41], v[168:171], v[192:195], v[38:41]
	v_mfma_f32_16x16x32_bf16 v[34:37], v[176:179], v[192:195], v[34:37]
	v_mfma_f32_16x16x32_bf16 v[22:25], v[168:171], v[200:203], v[22:25]
	v_mfma_f32_16x16x32_bf16 v[18:21], v[176:179], v[200:203], v[18:21]
	v_mfma_f32_16x16x32_bf16 v[6:9], v[168:171], v[208:211], v[6:9]
	v_mfma_f32_16x16x32_bf16 v[2:5], v[176:179], v[208:211], v[2:5]
	v_mfma_f32_16x16x32_bf16 v[54:57], v[172:175], v[188:191], v[54:57]
	v_mfma_f32_16x16x32_bf16 v[50:53], v[180:183], v[188:191], v[50:53]
	v_mfma_f32_16x16x32_bf16 v[38:41], v[172:175], v[196:199], v[38:41]
	v_mfma_f32_16x16x32_bf16 v[34:37], v[180:183], v[196:199], v[34:37]
	v_mfma_f32_16x16x32_bf16 v[22:25], v[172:175], v[204:207], v[22:25]
	v_mfma_f32_16x16x32_bf16 v[18:21], v[180:183], v[204:207], v[18:21]
	v_mfma_f32_16x16x32_bf16 v[6:9], v[172:175], v[212:215], v[6:9]
	v_mfma_f32_16x16x32_bf16 v[2:5], v[180:183], v[212:215], v[2:5]
	s_setprio 0
	s_barrier
	s_add_i32 s69, s69, 2
	s_add_u32 s22, s22, 0x100
	s_addc_u32 s23, s23, 0
	s_add_u32 s67, s67, 0x100
	s_addc_u32 s68, s68, 0
	s_cmp_gt_u32 s69, 29
	s_cbranch_scc0 .LBB0_574
	s_and_b64 vcc, exec, s[10:11]
	s_cbranch_vccz .LBB0_577
	s_barrier

.LBB0_659:
	ds_read_b128 v[150:153], v211
	ds_read_b128 v[154:157], v211 offset:1024
	ds_read_b128 v[158:161], v211 offset:2048
	ds_read_b128 v[162:165], v211 offset:3072
	ds_read_b128 v[166:169], v212
	ds_read_b128 v[170:173], v212 offset:1024
	ds_read_b128 v[174:177], v212 offset:2048
	ds_read_b128 v[178:181], v212 offset:3072
	s_add_u32 s36, s0, 0xffea8080
	s_addc_u32 s37, s1, -1
	s_cmpk_eq_i32 s44, 0x52
	s_cselect_b32 s43, s27, s37
	s_cselect_b32 s42, s26, s36
	s_cselect_b32 s37, s29, s35
	s_cselect_b32 s36, s28, s31
	s_add_i32 m0, s63, 0xc000
	ds_read_b128 v[182:185], v213
	ds_read_b128 v[186:189], v213 offset:1024
	ds_read_b128 v[190:193], v213 offset:2048
	ds_read_b128 v[194:197], v213 offset:3072
	ds_read_b128 v[198:201], v213 offset:4096
	ds_read_b128 v[202:205], v213 offset:5120
	ds_read_b128 v[218:221], v213 offset:6144
	ds_read_b128 v[222:225], v213 offset:7168
	global_load_lds_dwordx4 v142, s[0:1]
	s_add_i32 m0, s63, 0xe000
	s_nop 0
	global_load_lds_dwordx4 v144, s[0:1]
	s_waitcnt vmcnt(8)
	s_waitcnt lgkmcnt(0)
	s_barrier
	s_setprio 1
	s_waitcnt lgkmcnt(0)
	v_mfma_f32_16x16x32_bf16 v[126:129], v[150:153], v[182:185], v[126:129]
	v_mfma_f32_16x16x32_bf16 v[122:125], v[158:161], v[182:185], v[122:125]
	v_mfma_f32_16x16x32_bf16 v[110:113], v[150:153], v[190:193], v[110:113]
	v_mfma_f32_16x16x32_bf16 v[106:109], v[158:161], v[190:193], v[106:109]
	v_mfma_f32_16x16x32_bf16 v[94:97], v[150:153], v[198:201], v[94:97]
	v_mfma_f32_16x16x32_bf16 v[90:93], v[158:161], v[198:201], v[90:93]
	v_mfma_f32_16x16x32_bf16 v[78:81], v[150:153], v[218:221], v[78:81]
	v_mfma_f32_16x16x32_bf16 v[74:77], v[158:161], v[218:221], v[74:77]
	v_mfma_f32_16x16x32_bf16 v[126:129], v[154:157], v[186:189], v[126:129]
	v_mfma_f32_16x16x32_bf16 v[122:125], v[162:165], v[186:189], v[122:125]
	v_mfma_f32_16x16x32_bf16 v[110:113], v[154:157], v[194:197], v[110:113]
	v_mfma_f32_16x16x32_bf16 v[106:109], v[162:165], v[194:197], v[106:109]
	v_mfma_f32_16x16x32_bf16 v[94:97], v[154:157], v[202:205], v[94:97]
	v_mfma_f32_16x16x32_bf16 v[90:93], v[162:165], v[202:205], v[90:93]
	v_mfma_f32_16x16x32_bf16 v[78:81], v[154:157], v[222:225], v[78:81]
	v_mfma_f32_16x16x32_bf16 v[74:77], v[162:165], v[222:225], v[74:77]
	s_setprio 0
	s_setprio 1
	v_mfma_f32_16x16x32_bf16 v[118:121], v[166:169], v[182:185], v[118:121]
	v_mfma_f32_16x16x32_bf16 v[114:117], v[174:177], v[182:185], v[114:117]
	v_mfma_f32_16x16x32_bf16 v[102:105], v[166:169], v[190:193], v[102:105]
	v_mfma_f32_16x16x32_bf16 v[98:101], v[174:177], v[190:193], v[98:101]
	v_mfma_f32_16x16x32_bf16 v[86:89], v[166:169], v[198:201], v[86:89]
	v_mfma_f32_16x16x32_bf16 v[82:85], v[174:177], v[198:201], v[82:85]
	v_mfma_f32_16x16x32_bf16 v[70:73], v[166:169], v[218:221], v[70:73]
	v_mfma_f32_16x16x32_bf16 v[66:69], v[174:177], v[218:221], v[66:69]
	v_mfma_f32_16x16x32_bf16 v[118:121], v[170:173], v[186:189], v[118:121]
	v_mfma_f32_16x16x32_bf16 v[114:117], v[178:181], v[186:189], v[114:117]
	v_mfma_f32_16x16x32_bf16 v[102:105], v[170:173], v[194:197], v[102:105]
	v_mfma_f32_16x16x32_bf16 v[98:101], v[178:181], v[194:197], v[98:101]
	v_mfma_f32_16x16x32_bf16 v[86:89], v[170:173], v[202:205], v[86:89]
	v_mfma_f32_16x16x32_bf16 v[82:85], v[178:181], v[202:205], v[82:85]
	v_mfma_f32_16x16x32_bf16 v[70:73], v[170:173], v[222:225], v[70:73]
	v_mfma_f32_16x16x32_bf16 v[66:69], v[178:181], v[222:225], v[66:69]
	s_setprio 0
	s_barrier
	s_add_i32 s45, s75, s62
	s_mov_b32 m0, s45
	ds_read_b128 v[182:185], v213 offset:16384
	ds_read_b128 v[186:189], v213 offset:17408
	ds_read_b128 v[190:193], v213 offset:18432
	ds_read_b128 v[194:197], v213 offset:19456
	ds_read_b128 v[198:201], v213 offset:20480
	ds_read_b128 v[202:205], v213 offset:21504
	ds_read_b128 v[218:221], v213 offset:22528
	ds_read_b128 v[222:225], v213 offset:23552
	global_load_lds_dwordx4 v132, s[36:37]
	s_add_i32 m0, s45, 0x2000
	s_add_u32 s82, s36, 0x158000
	s_addc_u32 s83, s37, 0
	s_add_i32 s45, s76, s62
	global_load_lds_dwordx4 v136, s[36:37]
	s_mov_b32 m0, s45
	s_nop 0
	global_load_lds_dwordx4 v132, s[82:83]
	s_add_i32 m0, s45, 0x2000
	s_nop 0
	global_load_lds_dwordx4 v136, s[82:83]
	s_mov_b32 m0, s63
	s_nop 0
	global_load_lds_dwordx4 v130, s[42:43]
	s_mov_b32 m0, s64
	s_nop 0
	global_load_lds_dwordx4 v134, s[42:43]
	s_add_u32 s98, s36, 0x80
	s_addc_u32 s99, s37, 0
	s_add_u32 s100, s42, 0x80
	s_addc_u32 s101, s43, 0
	s_waitcnt vmcnt(8)
	s_waitcnt lgkmcnt(0)
	s_barrier
	s_setprio 1
	s_waitcnt lgkmcnt(0)
	v_mfma_f32_16x16x32_bf16 v[62:65], v[150:153], v[182:185], v[62:65]
	v_mfma_f32_16x16x32_bf16 v[58:61], v[158:161], v[182:185], v[58:61]
	v_mfma_f32_16x16x32_bf16 v[46:49], v[150:153], v[190:193], v[46:49]
	v_mfma_f32_16x16x32_bf16 v[42:45], v[158:161], v[190:193], v[42:45]
	v_mfma_f32_16x16x32_bf16 v[30:33], v[150:153], v[198:201], v[30:33]
	v_mfma_f32_16x16x32_bf16 v[26:29], v[158:161], v[198:201], v[26:29]
	v_mfma_f32_16x16x32_bf16 v[14:17], v[150:153], v[218:221], v[14:17]
	v_mfma_f32_16x16x32_bf16 v[10:13], v[158:161], v[218:221], v[10:13]
	v_mfma_f32_16x16x32_bf16 v[62:65], v[154:157], v[186:189], v[62:65]
	v_mfma_f32_16x16x32_bf16 v[58:61], v[162:165], v[186:189], v[58:61]
	v_mfma_f32_16x16x32_bf16 v[46:49], v[154:157], v[194:197], v[46:49]
	v_mfma_f32_16x16x32_bf16 v[42:45], v[162:165], v[194:197], v[42:45]
	v_mfma_f32_16x16x32_bf16 v[30:33], v[154:157], v[202:205], v[30:33]
	v_mfma_f32_16x16x32_bf16 v[26:29], v[162:165], v[202:205], v[26:29]
	v_mfma_f32_16x16x32_bf16 v[14:17], v[154:157], v[222:225], v[14:17]
	v_mfma_f32_16x16x32_bf16 v[10:13], v[162:165], v[222:225], v[10:13]
	s_setprio 0
	s_setprio 1
	v_mfma_f32_16x16x32_bf16 v[54:57], v[166:169], v[182:185], v[54:57]
	v_mfma_f32_16x16x32_bf16 v[50:53], v[174:177], v[182:185], v[50:53]
	v_mfma_f32_16x16x32_bf16 v[38:41], v[166:169], v[190:193], v[38:41]
	v_mfma_f32_16x16x32_bf16 v[34:37], v[174:177], v[190:193], v[34:37]
	v_mfma_f32_16x16x32_bf16 v[22:25], v[166:169], v[198:201], v[22:25]
	v_mfma_f32_16x16x32_bf16 v[18:21], v[174:177], v[198:201], v[18:21]
	v_mfma_f32_16x16x32_bf16 v[6:9], v[166:169], v[218:221], v[6:9]
	v_mfma_f32_16x16x32_bf16 v[2:5], v[174:177], v[218:221], v[2:5]
	v_mfma_f32_16x16x32_bf16 v[54:57], v[170:173], v[186:189], v[54:57]
	v_mfma_f32_16x16x32_bf16 v[50:53], v[178:181], v[186:189], v[50:53]
	v_mfma_f32_16x16x32_bf16 v[38:41], v[170:173], v[194:197], v[38:41]
	v_mfma_f32_16x16x32_bf16 v[34:37], v[178:181], v[194:197], v[34:37]
	v_mfma_f32_16x16x32_bf16 v[22:25], v[170:173], v[202:205], v[22:25]
	v_mfma_f32_16x16x32_bf16 v[18:21], v[178:181], v[202:205], v[18:21]
	v_mfma_f32_16x16x32_bf16 v[6:9], v[170:173], v[222:225], v[6:9]
	v_mfma_f32_16x16x32_bf16 v[2:5], v[178:181], v[222:225], v[2:5]
	s_setprio 0
	s_barrier
	s_add_i32 s45, 0, 0x18000
	v_add_u32_e32 v139, s45, v206
	s_add_i32 s81, 0, 0x1c000
	ds_read_b128 v[150:153], v139
	ds_read_b128 v[154:157], v139 offset:1024
	ds_read_b128 v[158:161], v139 offset:2048
	ds_read_b128 v[162:165], v139 offset:3072
	v_add_u32_e32 v139, s81, v206
	ds_read_b128 v[166:169], v139
	ds_read_b128 v[170:173], v139 offset:1024
	ds_read_b128 v[174:177], v139 offset:2048
	ds_read_b128 v[178:181], v139 offset:3072
	s_add_u32 s42, s42, 0x158000
	s_addc_u32 s43, s43, 0
	s_mov_b32 m0, s65
	ds_read_b128 v[182:185], v213 offset:32768
	ds_read_b128 v[186:189], v213 offset:33792
	ds_read_b128 v[190:193], v213 offset:34816
	ds_read_b128 v[194:197], v213 offset:35840
	ds_read_b128 v[198:201], v213 offset:36864
	ds_read_b128 v[202:205], v213 offset:37888
	ds_read_b128 v[218:221], v213 offset:38912
	ds_read_b128 v[222:225], v213 offset:39936
	global_load_lds_dwordx4 v130, s[42:43]
	s_mov_b32 m0, s66
	s_nop 0
	global_load_lds_dwordx4 v134, s[42:43]
	s_waitcnt vmcnt(8)
	s_waitcnt lgkmcnt(0)
	s_barrier
	s_setprio 1
	s_waitcnt lgkmcnt(0)
	v_mfma_f32_16x16x32_bf16 v[126:129], v[150:153], v[182:185], v[126:129]
	v_mfma_f32_16x16x32_bf16 v[122:125], v[158:161], v[182:185], v[122:125]
	v_mfma_f32_16x16x32_bf16 v[110:113], v[150:153], v[190:193], v[110:113]
	v_mfma_f32_16x16x32_bf16 v[106:109], v[158:161], v[190:193], v[106:109]
	v_mfma_f32_16x16x32_bf16 v[94:97], v[150:153], v[198:201], v[94:97]
	v_mfma_f32_16x16x32_bf16 v[90:93], v[158:161], v[198:201], v[90:93]
	v_mfma_f32_16x16x32_bf16 v[78:81], v[150:153], v[218:221], v[78:81]
	v_mfma_f32_16x16x32_bf16 v[74:77], v[158:161], v[218:221], v[74:77]
	v_mfma_f32_16x16x32_bf16 v[126:129], v[154:157], v[186:189], v[126:129]
	v_mfma_f32_16x16x32_bf16 v[122:125], v[162:165], v[186:189], v[122:125]
	v_mfma_f32_16x16x32_bf16 v[110:113], v[154:157], v[194:197], v[110:113]
	v_mfma_f32_16x16x32_bf16 v[106:109], v[162:165], v[194:197], v[106:109]
	v_mfma_f32_16x16x32_bf16 v[94:97], v[154:157], v[202:205], v[94:97]
	v_mfma_f32_16x16x32_bf16 v[90:93], v[162:165], v[202:205], v[90:93]
	v_mfma_f32_16x16x32_bf16 v[78:81], v[154:157], v[222:225], v[78:81]
	v_mfma_f32_16x16x32_bf16 v[74:77], v[162:165], v[222:225], v[74:77]
	s_setprio 0
	s_setprio 1
	v_mfma_f32_16x16x32_bf16 v[118:121], v[166:169], v[182:185], v[118:121]
	v_mfma_f32_16x16x32_bf16 v[114:117], v[174:177], v[182:185], v[114:117]
	v_mfma_f32_16x16x32_bf16 v[102:105], v[166:169], v[190:193], v[102:105]
	v_mfma_f32_16x16x32_bf16 v[98:101], v[174:177], v[190:193], v[98:101]
	v_mfma_f32_16x16x32_bf16 v[86:89], v[166:169], v[198:201], v[86:89]
	v_mfma_f32_16x16x32_bf16 v[82:85], v[174:177], v[198:201], v[82:85]
	v_mfma_f32_16x16x32_bf16 v[70:73], v[166:169], v[218:221], v[70:73]
	v_mfma_f32_16x16x32_bf16 v[66:69], v[174:177], v[218:221], v[66:69]
	v_mfma_f32_16x16x32_bf16 v[118:121], v[170:173], v[186:189], v[118:121]
	v_mfma_f32_16x16x32_bf16 v[114:117], v[178:181], v[186:189], v[114:117]
	v_mfma_f32_16x16x32_bf16 v[102:105], v[170:173], v[194:197], v[102:105]
	v_mfma_f32_16x16x32_bf16 v[98:101], v[178:181], v[194:197], v[98:101]
	v_mfma_f32_16x16x32_bf16 v[86:89], v[170:173], v[202:205], v[86:89]
	v_mfma_f32_16x16x32_bf16 v[82:85], v[178:181], v[202:205], v[82:85]
	v_mfma_f32_16x16x32_bf16 v[70:73], v[170:173], v[222:225], v[70:73]
	v_mfma_f32_16x16x32_bf16 v[66:69], v[178:181], v[222:225], v[66:69]
	s_setprio 0
	s_barrier
	s_add_i32 s42, s45, s62
	s_mov_b32 m0, s42
	ds_read_b128 v[182:185], v213 offset:49152
	ds_read_b128 v[186:189], v213 offset:50176
	ds_read_b128 v[190:193], v213 offset:51200
	ds_read_b128 v[194:197], v213 offset:52224
	ds_read_b128 v[198:201], v213 offset:53248
	ds_read_b128 v[202:205], v213 offset:54272
	ds_read_b128 v[218:221], v213 offset:55296
	ds_read_b128 v[222:225], v213 offset:56320
	global_load_lds_dwordx4 v132, s[98:99]
	s_add_i32 m0, s42, 0x2000
	s_add_u32 s36, s36, 0x158080
	s_addc_u32 s37, s37, 0
	s_add_i32 s42, s81, s62
	global_load_lds_dwordx4 v136, s[98:99]
	s_mov_b32 m0, s42
	s_nop 0
	global_load_lds_dwordx4 v132, s[36:37]
	s_add_i32 m0, s42, 0x2000
	s_nop 0
	global_load_lds_dwordx4 v136, s[36:37]
	s_mov_b32 m0, s70
	s_nop 0
	global_load_lds_dwordx4 v130, s[100:101]
	s_mov_b32 m0, s71
	s_nop 0
	global_load_lds_dwordx4 v134, s[100:101]
	s_waitcnt vmcnt(8)
	s_waitcnt lgkmcnt(0)
	s_barrier
	s_setprio 1
	s_waitcnt lgkmcnt(0)
	v_mfma_f32_16x16x32_bf16 v[62:65], v[150:153], v[182:185], v[62:65]
	v_mfma_f32_16x16x32_bf16 v[58:61], v[158:161], v[182:185], v[58:61]
	v_mfma_f32_16x16x32_bf16 v[46:49], v[150:153], v[190:193], v[46:49]
	v_mfma_f32_16x16x32_bf16 v[42:45], v[158:161], v[190:193], v[42:45]
	v_mfma_f32_16x16x32_bf16 v[30:33], v[150:153], v[198:201], v[30:33]
	v_mfma_f32_16x16x32_bf16 v[26:29], v[158:161], v[198:201], v[26:29]
	v_mfma_f32_16x16x32_bf16 v[14:17], v[150:153], v[218:221], v[14:17]
	v_mfma_f32_16x16x32_bf16 v[10:13], v[158:161], v[218:221], v[10:13]
	v_mfma_f32_16x16x32_bf16 v[62:65], v[154:157], v[186:189], v[62:65]
	v_mfma_f32_16x16x32_bf16 v[58:61], v[162:165], v[186:189], v[58:61]
	v_mfma_f32_16x16x32_bf16 v[46:49], v[154:157], v[194:197], v[46:49]
	v_mfma_f32_16x16x32_bf16 v[42:45], v[162:165], v[194:197], v[42:45]
	v_mfma_f32_16x16x32_bf16 v[30:33], v[154:157], v[202:205], v[30:33]
	v_mfma_f32_16x16x32_bf16 v[26:29], v[162:165], v[202:205], v[26:29]
	v_mfma_f32_16x16x32_bf16 v[14:17], v[154:157], v[222:225], v[14:17]
	v_mfma_f32_16x16x32_bf16 v[10:13], v[162:165], v[222:225], v[10:13]
	s_setprio 0
	s_setprio 1
	v_mfma_f32_16x16x32_bf16 v[54:57], v[166:169], v[182:185], v[54:57]
	v_mfma_f32_16x16x32_bf16 v[50:53], v[174:177], v[182:185], v[50:53]
	v_mfma_f32_16x16x32_bf16 v[38:41], v[166:169], v[190:193], v[38:41]
	v_mfma_f32_16x16x32_bf16 v[34:37], v[174:177], v[190:193], v[34:37]
	v_mfma_f32_16x16x32_bf16 v[22:25], v[166:169], v[198:201], v[22:25]
	v_mfma_f32_16x16x32_bf16 v[18:21], v[174:177], v[198:201], v[18:21]
	v_mfma_f32_16x16x32_bf16 v[6:9], v[166:169], v[218:221], v[6:9]
	v_mfma_f32_16x16x32_bf16 v[2:5], v[174:177], v[218:221], v[2:5]
	v_mfma_f32_16x16x32_bf16 v[54:57], v[170:173], v[186:189], v[54:57]
	v_mfma_f32_16x16x32_bf16 v[50:53], v[178:181], v[186:189], v[50:53]
	v_mfma_f32_16x16x32_bf16 v[38:41], v[170:173], v[194:197], v[38:41]
	v_mfma_f32_16x16x32_bf16 v[34:37], v[178:181], v[194:197], v[34:37]
	v_mfma_f32_16x16x32_bf16 v[22:25], v[170:173], v[202:205], v[22:25]
	v_mfma_f32_16x16x32_bf16 v[18:21], v[178:181], v[202:205], v[18:21]
	v_mfma_f32_16x16x32_bf16 v[6:9], v[170:173], v[222:225], v[6:9]
	v_mfma_f32_16x16x32_bf16 v[2:5], v[178:181], v[222:225], v[2:5]
	s_setprio 0
	s_barrier
	s_add_i32 s44, s44, 2
	s_add_u32 s0, s0, 0x100
	s_addc_u32 s1, s1, 0
	s_add_u32 s31, s31, 0x100
	s_addc_u32 s35, s35, 0
	s_cmpk_gt_u32 s44, 0x53
	s_cbranch_scc0 .LBB0_659
	s_and_b64 vcc, exec, s[22:23]
	s_cbranch_vccz .LBB0_662
	s_barrier

.LBB0_767:
	ds_read_b128 v[146:149], v152
	ds_read_b128 v[156:159], v152 offset:1024
	ds_read_b128 v[160:163], v152 offset:2048
	ds_read_b128 v[164:167], v152 offset:3072
	ds_read_b128 v[168:171], v153
	ds_read_b128 v[172:175], v153 offset:1024
	ds_read_b128 v[176:179], v153 offset:2048
	ds_read_b128 v[180:183], v153 offset:3072
	s_add_u32 s24, s22, 0xfff80080
	s_addc_u32 s25, s23, -1
	s_cmp_eq_u32 s69, 28
	s_cselect_b32 s27, s15, s25
	s_cselect_b32 s26, s65, s24
	s_cselect_b32 s25, s13, s68
	s_cselect_b32 s24, s66, s67
	s_add_i32 m0, s21, 0xc000
	ds_read_b128 v[184:187], v154
	ds_read_b128 v[188:191], v154 offset:1024
	ds_read_b128 v[192:195], v154 offset:2048
	ds_read_b128 v[196:199], v154 offset:3072
	ds_read_b128 v[200:203], v154 offset:4096
	ds_read_b128 v[204:207], v154 offset:5120
	ds_read_b128 v[208:211], v154 offset:6144
	ds_read_b128 v[212:215], v154 offset:7168
	global_load_lds_dwordx4 v138, s[22:23]
	s_add_i32 m0, s21, 0xe000
	s_nop 0
	global_load_lds_dwordx4 v140, s[22:23]
	s_waitcnt vmcnt(8)
	s_waitcnt lgkmcnt(0)
	s_barrier
	s_setprio 1
	s_waitcnt lgkmcnt(0)
	v_mfma_f32_16x16x32_bf16 v[126:129], v[146:149], v[184:187], v[126:129]
	v_mfma_f32_16x16x32_bf16 v[122:125], v[160:163], v[184:187], v[122:125]
	v_mfma_f32_16x16x32_bf16 v[118:121], v[146:149], v[192:195], v[118:121]
	v_mfma_f32_16x16x32_bf16 v[110:113], v[160:163], v[192:195], v[110:113]
	v_mfma_f32_16x16x32_bf16 v[102:105], v[146:149], v[200:203], v[102:105]
	v_mfma_f32_16x16x32_bf16 v[94:97], v[160:163], v[200:203], v[94:97]
	v_mfma_f32_16x16x32_bf16 v[86:89], v[146:149], v[208:211], v[86:89]
	v_mfma_f32_16x16x32_bf16 v[78:81], v[160:163], v[208:211], v[78:81]
	v_mfma_f32_16x16x32_bf16 v[126:129], v[156:159], v[188:191], v[126:129]
	v_mfma_f32_16x16x32_bf16 v[122:125], v[164:167], v[188:191], v[122:125]
	v_mfma_f32_16x16x32_bf16 v[118:121], v[156:159], v[196:199], v[118:121]
	v_mfma_f32_16x16x32_bf16 v[110:113], v[164:167], v[196:199], v[110:113]
	v_mfma_f32_16x16x32_bf16 v[102:105], v[156:159], v[204:207], v[102:105]
	v_mfma_f32_16x16x32_bf16 v[94:97], v[164:167], v[204:207], v[94:97]
	v_mfma_f32_16x16x32_bf16 v[86:89], v[156:159], v[212:215], v[86:89]
	v_mfma_f32_16x16x32_bf16 v[78:81], v[164:167], v[212:215], v[78:81]
	s_setprio 0
	s_setprio 1
	v_mfma_f32_16x16x32_bf16 v[114:117], v[168:171], v[184:187], v[114:117]
	v_mfma_f32_16x16x32_bf16 v[106:109], v[176:179], v[184:187], v[106:109]
	v_mfma_f32_16x16x32_bf16 v[98:101], v[168:171], v[192:195], v[98:101]
	v_mfma_f32_16x16x32_bf16 v[90:93], v[176:179], v[192:195], v[90:93]
	v_mfma_f32_16x16x32_bf16 v[82:85], v[168:171], v[200:203], v[82:85]
	v_mfma_f32_16x16x32_bf16 v[74:77], v[176:179], v[200:203], v[74:77]
	v_mfma_f32_16x16x32_bf16 v[70:73], v[168:171], v[208:211], v[70:73]
	v_mfma_f32_16x16x32_bf16 v[66:69], v[176:179], v[208:211], v[66:69]
	v_mfma_f32_16x16x32_bf16 v[114:117], v[172:175], v[188:191], v[114:117]
	v_mfma_f32_16x16x32_bf16 v[106:109], v[180:183], v[188:191], v[106:109]
	v_mfma_f32_16x16x32_bf16 v[98:101], v[172:175], v[196:199], v[98:101]
	v_mfma_f32_16x16x32_bf16 v[90:93], v[180:183], v[196:199], v[90:93]
	v_mfma_f32_16x16x32_bf16 v[82:85], v[172:175], v[204:207], v[82:85]
	v_mfma_f32_16x16x32_bf16 v[74:77], v[180:183], v[204:207], v[74:77]
	v_mfma_f32_16x16x32_bf16 v[70:73], v[172:175], v[212:215], v[70:73]
	v_mfma_f32_16x16x32_bf16 v[66:69], v[180:183], v[212:215], v[66:69]
	s_setprio 0
	s_barrier
	s_add_i32 s70, s61, s33
	s_mov_b32 m0, s70
	ds_read_b128 v[184:187], v154 offset:16384
	ds_read_b128 v[188:191], v154 offset:17408
	ds_read_b128 v[192:195], v154 offset:18432
	ds_read_b128 v[196:199], v154 offset:19456
	ds_read_b128 v[200:203], v154 offset:20480
	ds_read_b128 v[204:207], v154 offset:21504
	ds_read_b128 v[208:211], v154 offset:22528
	ds_read_b128 v[212:215], v154 offset:23552
	global_load_lds_dwordx4 v134, s[24:25]
	s_add_i32 m0, s70, 0x2000
	s_add_u32 s70, s24, 0x80000
	s_addc_u32 s71, s25, 0
	s_add_i32 s72, s62, s33
	global_load_lds_dwordx4 v130, s[24:25]
	s_mov_b32 m0, s72
	s_nop 0
	global_load_lds_dwordx4 v134, s[70:71]
	s_add_i32 m0, s72, 0x2000
	s_nop 0
	global_load_lds_dwordx4 v130, s[70:71]
	s_mov_b32 m0, s21
	s_nop 0
	global_load_lds_dwordx4 v136, s[26:27]
	s_mov_b32 m0, s36
	s_nop 0
	global_load_lds_dwordx4 v132, s[26:27]
	s_add_u32 s98, s24, 0x80
	s_addc_u32 s99, s25, 0
	s_add_u32 s100, s26, 0x80
	s_addc_u32 s101, s27, 0
	s_waitcnt vmcnt(8)
	s_waitcnt lgkmcnt(0)
	s_barrier
	s_setprio 1
	s_waitcnt lgkmcnt(0)
	v_mfma_f32_16x16x32_bf16 v[62:65], v[146:149], v[184:187], v[62:65]
	v_mfma_f32_16x16x32_bf16 v[58:61], v[160:163], v[184:187], v[58:61]
	v_mfma_f32_16x16x32_bf16 v[54:57], v[146:149], v[192:195], v[54:57]
	v_mfma_f32_16x16x32_bf16 v[46:49], v[160:163], v[192:195], v[46:49]
	v_mfma_f32_16x16x32_bf16 v[38:41], v[146:149], v[200:203], v[38:41]
	v_mfma_f32_16x16x32_bf16 v[30:33], v[160:163], v[200:203], v[30:33]
	v_mfma_f32_16x16x32_bf16 v[22:25], v[146:149], v[208:211], v[22:25]
	v_mfma_f32_16x16x32_bf16 v[14:17], v[160:163], v[208:211], v[14:17]
	v_mfma_f32_16x16x32_bf16 v[62:65], v[156:159], v[188:191], v[62:65]
	v_mfma_f32_16x16x32_bf16 v[58:61], v[164:167], v[188:191], v[58:61]
	v_mfma_f32_16x16x32_bf16 v[54:57], v[156:159], v[196:199], v[54:57]
	v_mfma_f32_16x16x32_bf16 v[46:49], v[164:167], v[196:199], v[46:49]
	v_mfma_f32_16x16x32_bf16 v[38:41], v[156:159], v[204:207], v[38:41]
	v_mfma_f32_16x16x32_bf16 v[30:33], v[164:167], v[204:207], v[30:33]
	v_mfma_f32_16x16x32_bf16 v[22:25], v[156:159], v[212:215], v[22:25]
	v_mfma_f32_16x16x32_bf16 v[14:17], v[164:167], v[212:215], v[14:17]
	s_setprio 0
	s_setprio 1
	v_mfma_f32_16x16x32_bf16 v[50:53], v[168:171], v[184:187], v[50:53]
	v_mfma_f32_16x16x32_bf16 v[42:45], v[176:179], v[184:187], v[42:45]
	v_mfma_f32_16x16x32_bf16 v[34:37], v[168:171], v[192:195], v[34:37]
	v_mfma_f32_16x16x32_bf16 v[26:29], v[176:179], v[192:195], v[26:29]
	v_mfma_f32_16x16x32_bf16 v[18:21], v[168:171], v[200:203], v[18:21]
	v_mfma_f32_16x16x32_bf16 v[10:13], v[176:179], v[200:203], v[10:13]
	v_mfma_f32_16x16x32_bf16 v[6:9], v[168:171], v[208:211], v[6:9]
	v_mfma_f32_16x16x32_bf16 v[2:5], v[176:179], v[208:211], v[2:5]
	v_mfma_f32_16x16x32_bf16 v[50:53], v[172:175], v[188:191], v[50:53]
	v_mfma_f32_16x16x32_bf16 v[42:45], v[180:183], v[188:191], v[42:45]
	v_mfma_f32_16x16x32_bf16 v[34:37], v[172:175], v[196:199], v[34:37]
	v_mfma_f32_16x16x32_bf16 v[26:29], v[180:183], v[196:199], v[26:29]
	v_mfma_f32_16x16x32_bf16 v[18:21], v[172:175], v[204:207], v[18:21]
	v_mfma_f32_16x16x32_bf16 v[10:13], v[180:183], v[204:207], v[10:13]
	v_mfma_f32_16x16x32_bf16 v[6:9], v[172:175], v[212:215], v[6:9]
	v_mfma_f32_16x16x32_bf16 v[2:5], v[180:183], v[212:215], v[2:5]
	s_setprio 0
	s_barrier
	s_add_i32 s70, 0, 0x18000
	v_add_u32_e32 v155, s70, v150
	s_add_i32 s71, 0, 0x1c000
	ds_read_b128 v[146:149], v155
	ds_read_b128 v[156:159], v155 offset:1024
	ds_read_b128 v[160:163], v155 offset:2048
	ds_read_b128 v[164:167], v155 offset:3072
	v_add_u32_e32 v155, s71, v150
	ds_read_b128 v[168:171], v155
	ds_read_b128 v[172:175], v155 offset:1024
	ds_read_b128 v[176:179], v155 offset:2048
	ds_read_b128 v[180:183], v155 offset:3072
	s_add_u32 s26, s26, 0x80000
	s_addc_u32 s27, s27, 0
	s_mov_b32 m0, s37
	ds_read_b128 v[184:187], v154 offset:32768
	ds_read_b128 v[188:191], v154 offset:33792
	ds_read_b128 v[192:195], v154 offset:34816
	ds_read_b128 v[196:199], v154 offset:35840
	ds_read_b128 v[200:203], v154 offset:36864
	ds_read_b128 v[204:207], v154 offset:37888
	ds_read_b128 v[208:211], v154 offset:38912
	ds_read_b128 v[212:215], v154 offset:39936
	global_load_lds_dwordx4 v136, s[26:27]
	s_mov_b32 m0, s42
	s_nop 0
	global_load_lds_dwordx4 v132, s[26:27]
	s_waitcnt vmcnt(8)
	s_waitcnt lgkmcnt(0)
	s_barrier
	s_setprio 1
	s_waitcnt lgkmcnt(0)
	v_mfma_f32_16x16x32_bf16 v[126:129], v[146:149], v[184:187], v[126:129]
	v_mfma_f32_16x16x32_bf16 v[122:125], v[160:163], v[184:187], v[122:125]
	v_mfma_f32_16x16x32_bf16 v[118:121], v[146:149], v[192:195], v[118:121]
	v_mfma_f32_16x16x32_bf16 v[110:113], v[160:163], v[192:195], v[110:113]
	v_mfma_f32_16x16x32_bf16 v[102:105], v[146:149], v[200:203], v[102:105]
	v_mfma_f32_16x16x32_bf16 v[94:97], v[160:163], v[200:203], v[94:97]
	v_mfma_f32_16x16x32_bf16 v[86:89], v[146:149], v[208:211], v[86:89]
	v_mfma_f32_16x16x32_bf16 v[78:81], v[160:163], v[208:211], v[78:81]
	v_mfma_f32_16x16x32_bf16 v[126:129], v[156:159], v[188:191], v[126:129]
	v_mfma_f32_16x16x32_bf16 v[122:125], v[164:167], v[188:191], v[122:125]
	v_mfma_f32_16x16x32_bf16 v[118:121], v[156:159], v[196:199], v[118:121]
	v_mfma_f32_16x16x32_bf16 v[110:113], v[164:167], v[196:199], v[110:113]
	v_mfma_f32_16x16x32_bf16 v[102:105], v[156:159], v[204:207], v[102:105]
	v_mfma_f32_16x16x32_bf16 v[94:97], v[164:167], v[204:207], v[94:97]
	v_mfma_f32_16x16x32_bf16 v[86:89], v[156:159], v[212:215], v[86:89]
	v_mfma_f32_16x16x32_bf16 v[78:81], v[164:167], v[212:215], v[78:81]
	s_setprio 0
	s_setprio 1
	v_mfma_f32_16x16x32_bf16 v[114:117], v[168:171], v[184:187], v[114:117]
	v_mfma_f32_16x16x32_bf16 v[106:109], v[176:179], v[184:187], v[106:109]
	v_mfma_f32_16x16x32_bf16 v[98:101], v[168:171], v[192:195], v[98:101]
	v_mfma_f32_16x16x32_bf16 v[90:93], v[176:179], v[192:195], v[90:93]
	v_mfma_f32_16x16x32_bf16 v[82:85], v[168:171], v[200:203], v[82:85]
	v_mfma_f32_16x16x32_bf16 v[74:77], v[176:179], v[200:203], v[74:77]
	v_mfma_f32_16x16x32_bf16 v[70:73], v[168:171], v[208:211], v[70:73]
	v_mfma_f32_16x16x32_bf16 v[66:69], v[176:179], v[208:211], v[66:69]
	v_mfma_f32_16x16x32_bf16 v[114:117], v[172:175], v[188:191], v[114:117]
	v_mfma_f32_16x16x32_bf16 v[106:109], v[180:183], v[188:191], v[106:109]
	v_mfma_f32_16x16x32_bf16 v[98:101], v[172:175], v[196:199], v[98:101]
	v_mfma_f32_16x16x32_bf16 v[90:93], v[180:183], v[196:199], v[90:93]
	v_mfma_f32_16x16x32_bf16 v[82:85], v[172:175], v[204:207], v[82:85]
	v_mfma_f32_16x16x32_bf16 v[74:77], v[180:183], v[204:207], v[74:77]
	v_mfma_f32_16x16x32_bf16 v[70:73], v[172:175], v[212:215], v[70:73]
	v_mfma_f32_16x16x32_bf16 v[66:69], v[180:183], v[212:215], v[66:69]
	s_setprio 0
	s_barrier
	s_add_i32 s26, s70, s33
	s_mov_b32 m0, s26
	ds_read_b128 v[184:187], v154 offset:49152
	ds_read_b128 v[188:191], v154 offset:50176
	ds_read_b128 v[192:195], v154 offset:51200
	ds_read_b128 v[196:199], v154 offset:52224
	ds_read_b128 v[200:203], v154 offset:53248
	ds_read_b128 v[204:207], v154 offset:54272
	ds_read_b128 v[208:211], v154 offset:55296
	ds_read_b128 v[212:215], v154 offset:56320
	global_load_lds_dwordx4 v134, s[98:99]
	s_add_i32 m0, s26, 0x2000
	s_add_u32 s24, s24, 0x80080
	s_addc_u32 s25, s25, 0
	s_add_i32 s26, s71, s33
	global_load_lds_dwordx4 v130, s[98:99]
	s_mov_b32 m0, s26
	s_nop 0
	global_load_lds_dwordx4 v134, s[24:25]
	s_add_i32 m0, s26, 0x2000
	s_nop 0
	global_load_lds_dwordx4 v130, s[24:25]
	s_mov_b32 m0, s44
	s_nop 0
	global_load_lds_dwordx4 v136, s[100:101]
	s_mov_b32 m0, s45
	s_nop 0
	global_load_lds_dwordx4 v132, s[100:101]
	s_waitcnt vmcnt(8)
	s_waitcnt lgkmcnt(0)
	s_barrier
	s_setprio 1
	s_waitcnt lgkmcnt(0)
	v_mfma_f32_16x16x32_bf16 v[62:65], v[146:149], v[184:187], v[62:65]
	v_mfma_f32_16x16x32_bf16 v[58:61], v[160:163], v[184:187], v[58:61]
	v_mfma_f32_16x16x32_bf16 v[54:57], v[146:149], v[192:195], v[54:57]
	v_mfma_f32_16x16x32_bf16 v[46:49], v[160:163], v[192:195], v[46:49]
	v_mfma_f32_16x16x32_bf16 v[38:41], v[146:149], v[200:203], v[38:41]
	v_mfma_f32_16x16x32_bf16 v[30:33], v[160:163], v[200:203], v[30:33]
	v_mfma_f32_16x16x32_bf16 v[22:25], v[146:149], v[208:211], v[22:25]
	v_mfma_f32_16x16x32_bf16 v[14:17], v[160:163], v[208:211], v[14:17]
	v_mfma_f32_16x16x32_bf16 v[62:65], v[156:159], v[188:191], v[62:65]
	v_mfma_f32_16x16x32_bf16 v[58:61], v[164:167], v[188:191], v[58:61]
	v_mfma_f32_16x16x32_bf16 v[54:57], v[156:159], v[196:199], v[54:57]
	v_mfma_f32_16x16x32_bf16 v[46:49], v[164:167], v[196:199], v[46:49]
	v_mfma_f32_16x16x32_bf16 v[38:41], v[156:159], v[204:207], v[38:41]
	v_mfma_f32_16x16x32_bf16 v[30:33], v[164:167], v[204:207], v[30:33]
	v_mfma_f32_16x16x32_bf16 v[22:25], v[156:159], v[212:215], v[22:25]
	v_mfma_f32_16x16x32_bf16 v[14:17], v[164:167], v[212:215], v[14:17]
	s_setprio 0
	s_setprio 1
	v_mfma_f32_16x16x32_bf16 v[50:53], v[168:171], v[184:187], v[50:53]
	v_mfma_f32_16x16x32_bf16 v[42:45], v[176:179], v[184:187], v[42:45]
	v_mfma_f32_16x16x32_bf16 v[34:37], v[168:171], v[192:195], v[34:37]
	v_mfma_f32_16x16x32_bf16 v[26:29], v[176:179], v[192:195], v[26:29]
	v_mfma_f32_16x16x32_bf16 v[18:21], v[168:171], v[200:203], v[18:21]
	v_mfma_f32_16x16x32_bf16 v[10:13], v[176:179], v[200:203], v[10:13]
	v_mfma_f32_16x16x32_bf16 v[6:9], v[168:171], v[208:211], v[6:9]
	v_mfma_f32_16x16x32_bf16 v[2:5], v[176:179], v[208:211], v[2:5]
	v_mfma_f32_16x16x32_bf16 v[50:53], v[172:175], v[188:191], v[50:53]
	v_mfma_f32_16x16x32_bf16 v[42:45], v[180:183], v[188:191], v[42:45]
	v_mfma_f32_16x16x32_bf16 v[34:37], v[172:175], v[196:199], v[34:37]
	v_mfma_f32_16x16x32_bf16 v[26:29], v[180:183], v[196:199], v[26:29]
	v_mfma_f32_16x16x32_bf16 v[18:21], v[172:175], v[204:207], v[18:21]
	v_mfma_f32_16x16x32_bf16 v[10:13], v[180:183], v[204:207], v[10:13]
	v_mfma_f32_16x16x32_bf16 v[6:9], v[172:175], v[212:215], v[6:9]
	v_mfma_f32_16x16x32_bf16 v[2:5], v[180:183], v[212:215], v[2:5]
	s_setprio 0
	s_barrier
	s_add_i32 s69, s69, 2
	s_add_u32 s22, s22, 0x100
	s_addc_u32 s23, s23, 0
	s_add_u32 s67, s67, 0x100
	s_addc_u32 s68, s68, 0
	s_cmp_gt_u32 s69, 29
	s_cbranch_scc0 .LBB0_767
	s_and_b64 vcc, exec, s[10:11]
	s_cbranch_vccz .LBB0_770
	s_barrier

.LBB0_1043:
	ds_read_b128 v[26:29], v209
	ds_read_b128 v[30:33], v209 offset:1024
	ds_read_b128 v[18:21], v209 offset:2048
	ds_read_b128 v[22:25], v209 offset:3072
	ds_read_b128 v[10:13], v210
	ds_read_b128 v[14:17], v210 offset:1024
	ds_read_b128 v[2:5], v210 offset:2048
	ds_read_b128 v[6:9], v210 offset:3072
	s_add_u32 s44, s40, 0xfffc0080
	s_addc_u32 s45, s41, -1
	s_cmp_eq_u32 s81, 12
	s_cselect_b32 s49, s1, s45
	s_cselect_b32 s48, s35, s44
	s_cselect_b32 s45, s31, s61
	s_cselect_b32 s44, s43, s60
	s_add_i32 m0, s65, 0xc000
	ds_read_b128 v[182:185], v211
	ds_read_b128 v[186:189], v211 offset:1024
	ds_read_b128 v[190:193], v211 offset:2048
	ds_read_b128 v[194:197], v211 offset:3072
	ds_read_b128 v[218:221], v211 offset:4096
	ds_read_b128 v[222:225], v211 offset:5120
	ds_read_b128 v[226:229], v211 offset:6144
	ds_read_b128 v[230:233], v211 offset:7168
	global_load_lds_dwordx4 v174, s[40:41]
	s_add_i32 m0, s65, 0xe000
	s_nop 0
	global_load_lds_dwordx4 v176, s[40:41]
	s_waitcnt vmcnt(8)
	s_waitcnt lgkmcnt(0)
	s_barrier
	s_setprio 1
	s_waitcnt lgkmcnt(0)
	v_mfma_scale_f32_16x16x128_f8f6f4 v[158:161], v[26:33], v[182:189], v[158:161], v212, v213 op_sel_hi:[0,0,0]
	v_mfma_scale_f32_16x16x128_f8f6f4 v[154:157], v[18:25], v[182:189], v[154:157], v212, v213 op_sel_hi:[0,0,0]
	v_mfma_scale_f32_16x16x128_f8f6f4 v[142:145], v[26:33], v[190:197], v[142:145], v212, v213 op_sel_hi:[0,0,0]
	v_mfma_scale_f32_16x16x128_f8f6f4 v[138:141], v[18:25], v[190:197], v[138:141], v212, v213 op_sel_hi:[0,0,0]
	v_mfma_scale_f32_16x16x128_f8f6f4 v[126:129], v[26:33], v[218:225], v[126:129], v212, v213 op_sel_hi:[0,0,0]
	v_mfma_scale_f32_16x16x128_f8f6f4 v[122:125], v[18:25], v[218:225], v[122:125], v212, v213 op_sel_hi:[0,0,0]
	v_mfma_scale_f32_16x16x128_f8f6f4 v[110:113], v[26:33], v[226:233], v[110:113], v212, v213 op_sel_hi:[0,0,0]
	v_mfma_scale_f32_16x16x128_f8f6f4 v[106:109], v[18:25], v[226:233], v[106:109], v212, v213 op_sel_hi:[0,0,0]
	s_setprio 0
	s_setprio 1
	v_mfma_scale_f32_16x16x128_f8f6f4 v[150:153], v[10:17], v[182:189], v[150:153], v212, v213 op_sel_hi:[0,0,0]
	v_mfma_scale_f32_16x16x128_f8f6f4 v[146:149], v[2:9], v[182:189], v[146:149], v212, v213 op_sel_hi:[0,0,0]
	v_mfma_scale_f32_16x16x128_f8f6f4 v[134:137], v[10:17], v[190:197], v[134:137], v212, v213 op_sel_hi:[0,0,0]
	v_mfma_scale_f32_16x16x128_f8f6f4 v[130:133], v[2:9], v[190:197], v[130:133], v212, v213 op_sel_hi:[0,0,0]
	v_mfma_scale_f32_16x16x128_f8f6f4 v[118:121], v[10:17], v[218:225], v[118:121], v212, v213 op_sel_hi:[0,0,0]
	v_mfma_scale_f32_16x16x128_f8f6f4 v[114:117], v[2:9], v[218:225], v[114:117], v212, v213 op_sel_hi:[0,0,0]
	v_mfma_scale_f32_16x16x128_f8f6f4 v[102:105], v[10:17], v[226:233], v[102:105], v212, v213 op_sel_hi:[0,0,0]
	v_mfma_scale_f32_16x16x128_f8f6f4 v[98:101], v[2:9], v[226:233], v[98:101], v212, v213 op_sel_hi:[0,0,0]
	s_setprio 0
	s_barrier
	s_add_i32 s82, s77, s64
	s_mov_b32 m0, s82
	ds_read_b128 v[190:193], v211 offset:16384
	ds_read_b128 v[194:197], v211 offset:17408
	ds_read_b128 v[218:221], v211 offset:18432
	ds_read_b128 v[222:225], v211 offset:19456
	ds_read_b128 v[226:229], v211 offset:20480
	ds_read_b128 v[230:233], v211 offset:21504
	ds_read_b128 v[234:237], v211 offset:22528
	ds_read_b128 v[238:241], v211 offset:23552
	global_load_lds_dwordx4 v164, s[44:45]
	s_add_i32 m0, s82, 0x2000
	s_add_u32 s82, s44, 0x40000
	s_addc_u32 s83, s45, 0
	s_add_i32 s84, s78, s64
	global_load_lds_dwordx4 v168, s[44:45]
	s_mov_b32 m0, s84
	s_nop 0
	global_load_lds_dwordx4 v164, s[82:83]
	s_add_i32 m0, s84, 0x2000
	s_nop 0
	global_load_lds_dwordx4 v168, s[82:83]
	s_mov_b32 m0, s65
	s_nop 0
	global_load_lds_dwordx4 v162, s[48:49]
	s_mov_b32 m0, s66
	s_nop 0
	global_load_lds_dwordx4 v166, s[48:49]
	s_add_u32 s98, s44, 0x80
	s_addc_u32 s99, s45, 0
	s_add_u32 s100, s48, 0x80
	s_addc_u32 s101, s49, 0
	s_waitcnt vmcnt(8)
	s_waitcnt lgkmcnt(0)
	s_barrier
	s_setprio 1
	s_waitcnt lgkmcnt(0)
	v_mfma_scale_f32_16x16x128_f8f6f4 v[94:97], v[26:33], v[190:197], v[94:97], v212, v213 op_sel_hi:[0,0,0]
	v_mfma_scale_f32_16x16x128_f8f6f4 v[90:93], v[18:25], v[190:197], v[90:93], v212, v213 op_sel_hi:[0,0,0]
	v_mfma_scale_f32_16x16x128_f8f6f4 v[78:81], v[26:33], v[218:225], v[78:81], v212, v213 op_sel_hi:[0,0,0]
	v_mfma_scale_f32_16x16x128_f8f6f4 v[74:77], v[18:25], v[218:225], v[74:77], v212, v213 op_sel_hi:[0,0,0]
	v_mfma_scale_f32_16x16x128_f8f6f4 v[62:65], v[26:33], v[226:233], v[62:65], v212, v213 op_sel_hi:[0,0,0]
	v_mfma_scale_f32_16x16x128_f8f6f4 v[58:61], v[18:25], v[226:233], v[58:61], v212, v213 op_sel_hi:[0,0,0]
	v_mfma_scale_f32_16x16x128_f8f6f4 v[46:49], v[26:33], v[234:241], v[46:49], v212, v213 op_sel_hi:[0,0,0]
	v_mfma_scale_f32_16x16x128_f8f6f4 v[42:45], v[18:25], v[234:241], v[42:45], v212, v213 op_sel_hi:[0,0,0]
	s_setprio 0
	s_setprio 1
	v_mfma_scale_f32_16x16x128_f8f6f4 v[86:89], v[10:17], v[190:197], v[86:89], v212, v213 op_sel_hi:[0,0,0]
	v_mfma_scale_f32_16x16x128_f8f6f4 v[82:85], v[2:9], v[190:197], v[82:85], v212, v213 op_sel_hi:[0,0,0]
	v_mfma_scale_f32_16x16x128_f8f6f4 v[70:73], v[10:17], v[218:225], v[70:73], v212, v213 op_sel_hi:[0,0,0]
	v_mfma_scale_f32_16x16x128_f8f6f4 v[66:69], v[2:9], v[218:225], v[66:69], v212, v213 op_sel_hi:[0,0,0]
	v_mfma_scale_f32_16x16x128_f8f6f4 v[54:57], v[10:17], v[226:233], v[54:57], v212, v213 op_sel_hi:[0,0,0]
	v_mfma_scale_f32_16x16x128_f8f6f4 v[50:53], v[2:9], v[226:233], v[50:53], v212, v213 op_sel_hi:[0,0,0]
	v_mfma_scale_f32_16x16x128_f8f6f4 v[38:41], v[10:17], v[234:241], v[38:41], v212, v213 op_sel_hi:[0,0,0]
	v_mfma_scale_f32_16x16x128_f8f6f4 v[34:37], v[2:9], v[234:241], v[34:37], v212, v213 op_sel_hi:[0,0,0]
	s_setprio 0
	s_barrier
	s_add_i32 s82, 0, 0x18000
	s_add_i32 s83, 0, 0x1c000
	v_add_u32_e32 v14, s82, v202
	v_add_u32_e32 v30, s83, v202
	ds_read_b128 v[2:5], v14
	ds_read_b128 v[6:9], v14 offset:1024
	ds_read_b128 v[10:13], v14 offset:2048
	ds_read_b128 v[14:17], v14 offset:3072
	ds_read_b128 v[18:21], v30
	ds_read_b128 v[22:25], v30 offset:1024
	ds_read_b128 v[26:29], v30 offset:2048
	ds_read_b128 v[30:33], v30 offset:3072
	s_add_u32 s48, s48, 0x40000
	s_addc_u32 s49, s49, 0
	s_mov_b32 m0, s67
	ds_read_b128 v[190:193], v211 offset:32768
	ds_read_b128 v[194:197], v211 offset:33792
	ds_read_b128 v[218:221], v211 offset:34816
	ds_read_b128 v[222:225], v211 offset:35840
	ds_read_b128 v[226:229], v211 offset:36864
	ds_read_b128 v[230:233], v211 offset:37888
	ds_read_b128 v[234:237], v211 offset:38912
	ds_read_b128 v[238:241], v211 offset:39936
	global_load_lds_dwordx4 v162, s[48:49]
	s_mov_b32 m0, s68
	s_nop 0
	global_load_lds_dwordx4 v166, s[48:49]
	s_waitcnt vmcnt(8)
	s_waitcnt lgkmcnt(0)
	s_barrier
	s_setprio 1
	s_waitcnt lgkmcnt(0)
	v_mfma_scale_f32_16x16x128_f8f6f4 v[158:161], v[2:9], v[190:197], v[158:161], v212, v213 op_sel_hi:[0,0,0]
	v_mfma_scale_f32_16x16x128_f8f6f4 v[154:157], v[10:17], v[190:197], v[154:157], v212, v213 op_sel_hi:[0,0,0]
	v_mfma_scale_f32_16x16x128_f8f6f4 v[142:145], v[2:9], v[218:225], v[142:145], v212, v213 op_sel_hi:[0,0,0]
	v_mfma_scale_f32_16x16x128_f8f6f4 v[138:141], v[10:17], v[218:225], v[138:141], v212, v213 op_sel_hi:[0,0,0]
	v_mfma_scale_f32_16x16x128_f8f6f4 v[126:129], v[2:9], v[226:233], v[126:129], v212, v213 op_sel_hi:[0,0,0]
	v_mfma_scale_f32_16x16x128_f8f6f4 v[122:125], v[10:17], v[226:233], v[122:125], v212, v213 op_sel_hi:[0,0,0]
	v_mfma_scale_f32_16x16x128_f8f6f4 v[110:113], v[2:9], v[234:241], v[110:113], v212, v213 op_sel_hi:[0,0,0]
	v_mfma_scale_f32_16x16x128_f8f6f4 v[106:109], v[10:17], v[234:241], v[106:109], v212, v213 op_sel_hi:[0,0,0]
	s_setprio 0
	s_setprio 1
	v_mfma_scale_f32_16x16x128_f8f6f4 v[150:153], v[18:25], v[190:197], v[150:153], v212, v213 op_sel_hi:[0,0,0]
	v_mfma_scale_f32_16x16x128_f8f6f4 v[146:149], v[26:33], v[190:197], v[146:149], v212, v213 op_sel_hi:[0,0,0]
	v_mfma_scale_f32_16x16x128_f8f6f4 v[134:137], v[18:25], v[218:225], v[134:137], v212, v213 op_sel_hi:[0,0,0]
	v_mfma_scale_f32_16x16x128_f8f6f4 v[130:133], v[26:33], v[218:225], v[130:133], v212, v213 op_sel_hi:[0,0,0]
	v_mfma_scale_f32_16x16x128_f8f6f4 v[118:121], v[18:25], v[226:233], v[118:121], v212, v213 op_sel_hi:[0,0,0]
	v_mfma_scale_f32_16x16x128_f8f6f4 v[114:117], v[26:33], v[226:233], v[114:117], v212, v213 op_sel_hi:[0,0,0]
	v_mfma_scale_f32_16x16x128_f8f6f4 v[102:105], v[18:25], v[234:241], v[102:105], v212, v213 op_sel_hi:[0,0,0]
	v_mfma_scale_f32_16x16x128_f8f6f4 v[98:101], v[26:33], v[234:241], v[98:101], v212, v213 op_sel_hi:[0,0,0]
	s_setprio 0
	s_barrier
	s_add_i32 s48, s82, s64
	s_mov_b32 m0, s48
	ds_read_b128 v[190:193], v211 offset:49152
	ds_read_b128 v[194:197], v211 offset:50176
	ds_read_b128 v[218:221], v211 offset:51200
	ds_read_b128 v[222:225], v211 offset:52224
	ds_read_b128 v[226:229], v211 offset:53248
	ds_read_b128 v[230:233], v211 offset:54272
	ds_read_b128 v[234:237], v211 offset:55296
	ds_read_b128 v[238:241], v211 offset:56320
	global_load_lds_dwordx4 v164, s[98:99]
	s_add_i32 m0, s48, 0x2000
	s_add_u32 s44, s44, 0x40080
	s_addc_u32 s45, s45, 0
	s_add_i32 s48, s83, s64
	global_load_lds_dwordx4 v168, s[98:99]
	s_mov_b32 m0, s48
	s_nop 0
	global_load_lds_dwordx4 v164, s[44:45]
	s_add_i32 m0, s48, 0x2000
	s_nop 0
	global_load_lds_dwordx4 v168, s[44:45]
	s_mov_b32 m0, s72
	s_nop 0
	global_load_lds_dwordx4 v162, s[100:101]
	s_mov_b32 m0, s73
	s_nop 0
	global_load_lds_dwordx4 v166, s[100:101]
	s_waitcnt vmcnt(8)
	s_waitcnt lgkmcnt(0)
	s_barrier
	s_setprio 1
	s_waitcnt lgkmcnt(0)
	v_mfma_scale_f32_16x16x128_f8f6f4 v[94:97], v[2:9], v[190:197], v[94:97], v212, v213 op_sel_hi:[0,0,0]
	v_mfma_scale_f32_16x16x128_f8f6f4 v[90:93], v[10:17], v[190:197], v[90:93], v212, v213 op_sel_hi:[0,0,0]
	v_mfma_scale_f32_16x16x128_f8f6f4 v[78:81], v[2:9], v[218:225], v[78:81], v212, v213 op_sel_hi:[0,0,0]
	v_mfma_scale_f32_16x16x128_f8f6f4 v[74:77], v[10:17], v[218:225], v[74:77], v212, v213 op_sel_hi:[0,0,0]
	v_mfma_scale_f32_16x16x128_f8f6f4 v[62:65], v[2:9], v[226:233], v[62:65], v212, v213 op_sel_hi:[0,0,0]
	v_mfma_scale_f32_16x16x128_f8f6f4 v[58:61], v[10:17], v[226:233], v[58:61], v212, v213 op_sel_hi:[0,0,0]
	v_mfma_scale_f32_16x16x128_f8f6f4 v[46:49], v[2:9], v[234:241], v[46:49], v212, v213 op_sel_hi:[0,0,0]
	v_mfma_scale_f32_16x16x128_f8f6f4 v[42:45], v[10:17], v[234:241], v[42:45], v212, v213 op_sel_hi:[0,0,0]
	s_setprio 0
	s_setprio 1
	v_mfma_scale_f32_16x16x128_f8f6f4 v[86:89], v[18:25], v[190:197], v[86:89], v212, v213 op_sel_hi:[0,0,0]
	v_mfma_scale_f32_16x16x128_f8f6f4 v[82:85], v[26:33], v[190:197], v[82:85], v212, v213 op_sel_hi:[0,0,0]
	v_mfma_scale_f32_16x16x128_f8f6f4 v[70:73], v[18:25], v[218:225], v[70:73], v212, v213 op_sel_hi:[0,0,0]
	v_mfma_scale_f32_16x16x128_f8f6f4 v[66:69], v[26:33], v[218:225], v[66:69], v212, v213 op_sel_hi:[0,0,0]
	v_mfma_scale_f32_16x16x128_f8f6f4 v[54:57], v[18:25], v[226:233], v[54:57], v212, v213 op_sel_hi:[0,0,0]
	v_mfma_scale_f32_16x16x128_f8f6f4 v[50:53], v[26:33], v[226:233], v[50:53], v212, v213 op_sel_hi:[0,0,0]
	v_mfma_scale_f32_16x16x128_f8f6f4 v[38:41], v[18:25], v[234:241], v[38:41], v212, v213 op_sel_hi:[0,0,0]
	v_mfma_scale_f32_16x16x128_f8f6f4 v[34:37], v[26:33], v[234:241], v[34:37], v212, v213 op_sel_hi:[0,0,0]
	s_setprio 0
	s_barrier
	s_add_i32 s81, s81, 2
	s_add_u32 s40, s40, 0x100
	s_addc_u32 s41, s41, 0
	s_add_u32 s60, s60, 0x100
	s_addc_u32 s61, s61, 0
	s_cmp_gt_u32 s81, 13
	s_cbranch_scc0 .LBB0_1043
	s_and_b64 vcc, exec, s[26:27]
	s_cbranch_vccz .LBB0_1046
	s_barrier

.LBB0_1257:
	ds_read_b128 v[20:23], v202
	ds_read_b128 v[166:169], v202 offset:1024
	ds_read_b128 v[14:17], v202 offset:2048
	ds_read_b128 v[162:165], v202 offset:3072
	ds_read_b128 v[8:11], v203
	ds_read_b128 v[158:161], v203 offset:1024
	ds_read_b128 v[2:5], v203 offset:2048
	ds_read_b128 v[154:157], v203 offset:3072
	s_add_u32 s22, s20, 0xfffc0080
	s_addc_u32 s23, s21, -1
	s_cmp_eq_u32 s63, 12
	s_cselect_b32 s25, s11, s23
	s_cselect_b32 s24, s49, s22
	s_cselect_b32 s23, s13, s62
	s_cselect_b32 s22, s60, s61
	s_add_i32 m0, s35, 0xc000
	ds_read_b128 v[184:187], v204
	ds_read_b128 v[188:191], v204 offset:1024
	ds_read_b128 v[206:209], v204 offset:2048
	ds_read_b128 v[222:225], v204 offset:3072
	ds_read_b128 v[212:215], v204 offset:4096
	ds_read_b128 v[226:229], v204 offset:5120
	ds_read_b128 v[218:221], v204 offset:6144
	ds_read_b128 v[230:233], v204 offset:7168
	global_load_lds_dwordx4 v180, s[20:21]
	s_add_i32 m0, s35, 0xe000
	s_nop 0
	global_load_lds_dwordx4 v182, s[20:21]
	s_waitcnt vmcnt(8)
	s_waitcnt lgkmcnt(0)
	s_barrier
	s_setprio 1
	s_waitcnt lgkmcnt(0)
	v_mov_b32_e32 v24, v166
	v_mov_b32_e32 v25, v167
	s_nop 1
	v_mfma_scale_f32_16x16x128_f8f6f4 v[150:153], v[20:25], v[184:189], v[150:153], v168, v190 op_sel_hi:[0,0,0] cbsz:2 blgp:2
	v_mov_b32_e32 v18, v162
	v_mov_b32_e32 v19, v163
	s_nop 1
	v_mfma_scale_f32_16x16x128_f8f6f4 v[138:141], v[14:19], v[184:189], v[138:141], v164, v190 op_sel_hi:[0,0,0] cbsz:2 blgp:2
	v_mov_b32_e32 v210, v222
	v_mov_b32_e32 v211, v223
	s_nop 1
	v_mfma_scale_f32_16x16x128_f8f6f4 v[134:137], v[20:25], v[206:211], v[134:137], v168, v224 op_sel_hi:[0,0,0] cbsz:2 blgp:2
	s_nop 1
	v_mfma_scale_f32_16x16x128_f8f6f4 v[122:125], v[14:19], v[206:211], v[122:125], v164, v224 op_sel_hi:[0,0,0] cbsz:2 blgp:2
	v_mov_b32_e32 v216, v226
	v_mov_b32_e32 v217, v227
	s_nop 1
	v_mfma_scale_f32_16x16x128_f8f6f4 v[118:121], v[20:25], v[212:217], v[118:121], v168, v228 op_sel_hi:[0,0,0] cbsz:2 blgp:2
	s_nop 1
	v_mfma_scale_f32_16x16x128_f8f6f4 v[106:109], v[14:19], v[212:217], v[106:109], v164, v228 op_sel_hi:[0,0,0] cbsz:2 blgp:2
	v_mov_b32_e32 v222, v230
	v_mov_b32_e32 v223, v231
	s_nop 1
	v_mfma_scale_f32_16x16x128_f8f6f4 v[102:105], v[20:25], v[218:223], v[102:105], v168, v232 op_sel_hi:[0,0,0] cbsz:2 blgp:2
	s_nop 1
	v_mfma_scale_f32_16x16x128_f8f6f4 v[90:93], v[14:19], v[218:223], v[90:93], v164, v232 op_sel_hi:[0,0,0] cbsz:2 blgp:2
	s_setprio 0
	s_setprio 1
	v_mov_b32_e32 v12, v158
	v_mov_b32_e32 v13, v159
	s_nop 1
	v_mfma_scale_f32_16x16x128_f8f6f4 v[146:149], v[8:13], v[184:189], v[146:149], v160, v190 op_sel_hi:[0,0,0] cbsz:2 blgp:2
	v_mov_b32_e32 v6, v154
	v_mov_b32_e32 v7, v155
	s_nop 1
	v_mfma_scale_f32_16x16x128_f8f6f4 v[142:145], v[2:7], v[184:189], v[142:145], v156, v190 op_sel_hi:[0,0,0] cbsz:2 blgp:2
	s_nop 1
	v_mfma_scale_f32_16x16x128_f8f6f4 v[130:133], v[8:13], v[206:211], v[130:133], v160, v224 op_sel_hi:[0,0,0] cbsz:2 blgp:2
	s_nop 1
	v_mfma_scale_f32_16x16x128_f8f6f4 v[126:129], v[2:7], v[206:211], v[126:129], v156, v224 op_sel_hi:[0,0,0] cbsz:2 blgp:2
	s_nop 1
	v_mfma_scale_f32_16x16x128_f8f6f4 v[114:117], v[8:13], v[212:217], v[114:117], v160, v228 op_sel_hi:[0,0,0] cbsz:2 blgp:2
	s_nop 1
	v_mfma_scale_f32_16x16x128_f8f6f4 v[110:113], v[2:7], v[212:217], v[110:113], v156, v228 op_sel_hi:[0,0,0] cbsz:2 blgp:2
	s_nop 1
	v_mfma_scale_f32_16x16x128_f8f6f4 v[98:101], v[8:13], v[218:223], v[98:101], v160, v232 op_sel_hi:[0,0,0] cbsz:2 blgp:2
	s_nop 1
	v_mfma_scale_f32_16x16x128_f8f6f4 v[94:97], v[2:7], v[218:223], v[94:97], v156, v232 op_sel_hi:[0,0,0] cbsz:2 blgp:2
	s_setprio 0
	s_barrier
	s_add_i32 s64, s42, s27
	s_mov_b32 m0, s64
	ds_read_b128 v[206:209], v204 offset:16384
	ds_read_b128 v[228:231], v204 offset:17408
	ds_read_b128 v[212:215], v204 offset:18432
	ds_read_b128 v[232:235], v204 offset:19456
	ds_read_b128 v[218:221], v204 offset:20480
	ds_read_b128 v[236:239], v204 offset:21504
	ds_read_b128 v[224:227], v204 offset:22528
	ds_read_b128 v[240:243], v204 offset:23552
	global_load_lds_dwordx4 v172, s[22:23]
	s_add_i32 m0, s64, 0x2000
	s_add_u32 s64, s22, 0x40000
	s_addc_u32 s65, s23, 0
	s_add_i32 s66, s43, s27
	global_load_lds_dwordx4 v174, s[22:23]
	s_mov_b32 m0, s66
	s_nop 0
	global_load_lds_dwordx4 v172, s[64:65]
	s_add_i32 m0, s66, 0x2000
	s_nop 0
	global_load_lds_dwordx4 v174, s[64:65]
	s_mov_b32 m0, s35
	s_nop 0
	global_load_lds_dwordx4 v178, s[24:25]
	s_mov_b32 m0, s36
	s_nop 0
	global_load_lds_dwordx4 v176, s[24:25]
	s_add_u32 s98, s22, 0x80
	s_addc_u32 s99, s23, 0
	s_add_u32 s100, s24, 0x80
	s_addc_u32 s101, s25, 0
	s_waitcnt vmcnt(8)
	s_waitcnt lgkmcnt(0)
	s_barrier
	s_setprio 1
	s_waitcnt lgkmcnt(0)
	v_mov_b32_e32 v210, v228
	v_mov_b32_e32 v211, v229
	s_nop 1
	v_mfma_scale_f32_16x16x128_f8f6f4 v[86:89], v[20:25], v[206:211], v[86:89], v168, v230 op_sel_hi:[0,0,0] cbsz:2 blgp:2
	s_nop 1
	v_mfma_scale_f32_16x16x128_f8f6f4 v[74:77], v[14:19], v[206:211], v[74:77], v164, v230 op_sel_hi:[0,0,0] cbsz:2 blgp:2
	v_mov_b32_e32 v216, v232
	v_mov_b32_e32 v217, v233
	s_nop 1
	v_mfma_scale_f32_16x16x128_f8f6f4 v[70:73], v[20:25], v[212:217], v[70:73], v168, v234 op_sel_hi:[0,0,0] cbsz:2 blgp:2
	s_nop 1
	v_mfma_scale_f32_16x16x128_f8f6f4 v[58:61], v[14:19], v[212:217], v[58:61], v164, v234 op_sel_hi:[0,0,0] cbsz:2 blgp:2
	v_mov_b32_e32 v222, v236
	v_mov_b32_e32 v223, v237
	s_nop 1
	v_mfma_scale_f32_16x16x128_f8f6f4 v[54:57], v[20:25], v[218:223], v[54:57], v168, v238 op_sel_hi:[0,0,0] cbsz:2 blgp:2
	s_nop 1
	v_mfma_scale_f32_16x16x128_f8f6f4 v[42:45], v[14:19], v[218:223], v[42:45], v164, v238 op_sel_hi:[0,0,0] cbsz:2 blgp:2
	v_mov_b32_e32 v228, v240
	v_mov_b32_e32 v229, v241
	s_nop 1
	v_mfma_scale_f32_16x16x128_f8f6f4 v[38:41], v[20:25], v[224:229], v[38:41], v168, v242 op_sel_hi:[0,0,0] cbsz:2 blgp:2
	s_nop 1
	v_mfma_scale_f32_16x16x128_f8f6f4 v[26:29], v[14:19], v[224:229], v[26:29], v164, v242 op_sel_hi:[0,0,0] cbsz:2 blgp:2
	s_setprio 0
	s_setprio 1
	s_nop 1
	v_mfma_scale_f32_16x16x128_f8f6f4 v[82:85], v[8:13], v[206:211], v[82:85], v160, v230 op_sel_hi:[0,0,0] cbsz:2 blgp:2
	s_nop 1
	v_mfma_scale_f32_16x16x128_f8f6f4 v[78:81], v[2:7], v[206:211], v[78:81], v156, v230 op_sel_hi:[0,0,0] cbsz:2 blgp:2
	s_nop 1
	v_mfma_scale_f32_16x16x128_f8f6f4 v[66:69], v[8:13], v[212:217], v[66:69], v160, v234 op_sel_hi:[0,0,0] cbsz:2 blgp:2
	s_nop 1
	v_mfma_scale_f32_16x16x128_f8f6f4 v[62:65], v[2:7], v[212:217], v[62:65], v156, v234 op_sel_hi:[0,0,0] cbsz:2 blgp:2
	s_nop 1
	v_mfma_scale_f32_16x16x128_f8f6f4 v[50:53], v[8:13], v[218:223], v[50:53], v160, v238 op_sel_hi:[0,0,0] cbsz:2 blgp:2
	s_nop 1
	v_mfma_scale_f32_16x16x128_f8f6f4 v[46:49], v[2:7], v[218:223], v[46:49], v156, v238 op_sel_hi:[0,0,0] cbsz:2 blgp:2
	s_nop 1
	v_mfma_scale_f32_16x16x128_f8f6f4 v[34:37], v[8:13], v[224:229], v[34:37], v160, v242 op_sel_hi:[0,0,0] cbsz:2 blgp:2
	s_nop 1
	v_mfma_scale_f32_16x16x128_f8f6f4 v[30:33], v[2:7], v[224:229], v[30:33], v156, v242 op_sel_hi:[0,0,0] cbsz:2 blgp:2
	s_setprio 0
	s_barrier
	s_add_i32 s64, 0, 0x18000
	s_add_i32 s65, 0, 0x1c000
	v_add_u32_e32 v2, s64, v198
	v_add_u32_e32 v6, s65, v198
	ds_read_b128 v[20:23], v2
	ds_read_b128 v[166:169], v2 offset:1024
	ds_read_b128 v[14:17], v2 offset:2048
	ds_read_b128 v[162:165], v2 offset:3072
	ds_read_b128 v[8:11], v6
	ds_read_b128 v[154:157], v6 offset:1024
	ds_read_b128 v[2:5], v6 offset:2048
	ds_read_b128 v[158:161], v6 offset:3072
	s_add_u32 s24, s24, 0x40000
	s_addc_u32 s25, s25, 0
	s_mov_b32 m0, s37
	ds_read_b128 v[206:209], v204 offset:32768
	ds_read_b128 v[228:231], v204 offset:33792
	ds_read_b128 v[212:215], v204 offset:34816
	ds_read_b128 v[232:235], v204 offset:35840
	ds_read_b128 v[218:221], v204 offset:36864
	ds_read_b128 v[236:239], v204 offset:37888
	ds_read_b128 v[224:227], v204 offset:38912
	ds_read_b128 v[240:243], v204 offset:39936
	global_load_lds_dwordx4 v178, s[24:25]
	s_mov_b32 m0, s38
	s_nop 0
	global_load_lds_dwordx4 v176, s[24:25]
	s_waitcnt vmcnt(8)
	s_waitcnt lgkmcnt(0)
	s_barrier
	s_setprio 1
	s_waitcnt lgkmcnt(0)
	v_mov_b32_e32 v24, v166
	v_mov_b32_e32 v25, v167
	v_mov_b32_e32 v210, v228
	v_mov_b32_e32 v211, v229
	s_nop 1
	v_mfma_scale_f32_16x16x128_f8f6f4 v[150:153], v[20:25], v[206:211], v[150:153], v168, v230 op_sel_hi:[0,0,0] cbsz:2 blgp:2
	v_mov_b32_e32 v18, v162
	v_mov_b32_e32 v19, v163
	s_nop 1
	v_mfma_scale_f32_16x16x128_f8f6f4 v[138:141], v[14:19], v[206:211], v[138:141], v164, v230 op_sel_hi:[0,0,0] cbsz:2 blgp:2
	v_mov_b32_e32 v216, v232
	v_mov_b32_e32 v217, v233
	s_nop 1
	v_mfma_scale_f32_16x16x128_f8f6f4 v[134:137], v[20:25], v[212:217], v[134:137], v168, v234 op_sel_hi:[0,0,0] cbsz:2 blgp:2
	s_nop 1
	v_mfma_scale_f32_16x16x128_f8f6f4 v[122:125], v[14:19], v[212:217], v[122:125], v164, v234 op_sel_hi:[0,0,0] cbsz:2 blgp:2
	v_mov_b32_e32 v222, v236
	v_mov_b32_e32 v223, v237
	s_nop 1
	v_mfma_scale_f32_16x16x128_f8f6f4 v[118:121], v[20:25], v[218:223], v[118:121], v168, v238 op_sel_hi:[0,0,0] cbsz:2 blgp:2
	s_nop 1
	v_mfma_scale_f32_16x16x128_f8f6f4 v[106:109], v[14:19], v[218:223], v[106:109], v164, v238 op_sel_hi:[0,0,0] cbsz:2 blgp:2
	v_mov_b32_e32 v228, v240
	v_mov_b32_e32 v229, v241
	s_nop 1
	v_mfma_scale_f32_16x16x128_f8f6f4 v[102:105], v[20:25], v[224:229], v[102:105], v168, v242 op_sel_hi:[0,0,0] cbsz:2 blgp:2
	s_nop 1
	v_mfma_scale_f32_16x16x128_f8f6f4 v[90:93], v[14:19], v[224:229], v[90:93], v164, v242 op_sel_hi:[0,0,0] cbsz:2 blgp:2
	s_setprio 0
	s_setprio 1
	v_mov_b32_e32 v12, v154
	v_mov_b32_e32 v13, v155
	s_nop 1
	v_mfma_scale_f32_16x16x128_f8f6f4 v[146:149], v[8:13], v[206:211], v[146:149], v156, v230 op_sel_hi:[0,0,0] cbsz:2 blgp:2
	v_mov_b32_e32 v6, v158
	v_mov_b32_e32 v7, v159
	s_nop 1
	v_mfma_scale_f32_16x16x128_f8f6f4 v[142:145], v[2:7], v[206:211], v[142:145], v160, v230 op_sel_hi:[0,0,0] cbsz:2 blgp:2
	s_nop 1
	v_mfma_scale_f32_16x16x128_f8f6f4 v[130:133], v[8:13], v[212:217], v[130:133], v156, v234 op_sel_hi:[0,0,0] cbsz:2 blgp:2
	s_nop 1
	v_mfma_scale_f32_16x16x128_f8f6f4 v[126:129], v[2:7], v[212:217], v[126:129], v160, v234 op_sel_hi:[0,0,0] cbsz:2 blgp:2
	s_nop 1
	v_mfma_scale_f32_16x16x128_f8f6f4 v[114:117], v[8:13], v[218:223], v[114:117], v156, v238 op_sel_hi:[0,0,0] cbsz:2 blgp:2
	s_nop 1
	v_mfma_scale_f32_16x16x128_f8f6f4 v[110:113], v[2:7], v[218:223], v[110:113], v160, v238 op_sel_hi:[0,0,0] cbsz:2 blgp:2
	s_nop 1
	v_mfma_scale_f32_16x16x128_f8f6f4 v[98:101], v[8:13], v[224:229], v[98:101], v156, v242 op_sel_hi:[0,0,0] cbsz:2 blgp:2
	s_nop 1
	v_mfma_scale_f32_16x16x128_f8f6f4 v[94:97], v[2:7], v[224:229], v[94:97], v160, v242 op_sel_hi:[0,0,0] cbsz:2 blgp:2
	s_setprio 0
	s_barrier
	s_add_i32 s24, s64, s27
	s_mov_b32 m0, s24
	ds_read_b128 v[206:209], v204 offset:49152
	ds_read_b128 v[228:231], v204 offset:50176
	ds_read_b128 v[212:215], v204 offset:51200
	ds_read_b128 v[232:235], v204 offset:52224
	ds_read_b128 v[218:221], v204 offset:53248
	ds_read_b128 v[236:239], v204 offset:54272
	ds_read_b128 v[224:227], v204 offset:55296
	ds_read_b128 v[240:243], v204 offset:56320
	global_load_lds_dwordx4 v172, s[98:99]
	s_add_i32 m0, s24, 0x2000
	s_add_u32 s22, s22, 0x40080
	s_addc_u32 s23, s23, 0
	s_add_i32 s24, s65, s27
	global_load_lds_dwordx4 v174, s[98:99]
	s_mov_b32 m0, s24
	s_nop 0
	global_load_lds_dwordx4 v172, s[22:23]
	s_add_i32 m0, s24, 0x2000
	s_nop 0
	global_load_lds_dwordx4 v174, s[22:23]
	s_mov_b32 m0, s39
	s_nop 0
	global_load_lds_dwordx4 v178, s[100:101]
	s_mov_b32 m0, s40
	s_nop 0
	global_load_lds_dwordx4 v176, s[100:101]
	s_waitcnt vmcnt(8)
	s_waitcnt lgkmcnt(0)
	s_barrier
	s_setprio 1
	s_waitcnt lgkmcnt(0)
	v_mov_b32_e32 v210, v228
	v_mov_b32_e32 v211, v229
	s_nop 1
	v_mfma_scale_f32_16x16x128_f8f6f4 v[86:89], v[20:25], v[206:211], v[86:89], v168, v230 op_sel_hi:[0,0,0] cbsz:2 blgp:2
	s_nop 1
	v_mfma_scale_f32_16x16x128_f8f6f4 v[74:77], v[14:19], v[206:211], v[74:77], v164, v230 op_sel_hi:[0,0,0] cbsz:2 blgp:2
	v_mov_b32_e32 v216, v232
	v_mov_b32_e32 v217, v233
	s_nop 1
	v_mfma_scale_f32_16x16x128_f8f6f4 v[70:73], v[20:25], v[212:217], v[70:73], v168, v234 op_sel_hi:[0,0,0] cbsz:2 blgp:2
	s_nop 1
	v_mfma_scale_f32_16x16x128_f8f6f4 v[58:61], v[14:19], v[212:217], v[58:61], v164, v234 op_sel_hi:[0,0,0] cbsz:2 blgp:2
	v_mov_b32_e32 v222, v236
	v_mov_b32_e32 v223, v237
	s_nop 1
	v_mfma_scale_f32_16x16x128_f8f6f4 v[54:57], v[20:25], v[218:223], v[54:57], v168, v238 op_sel_hi:[0,0,0] cbsz:2 blgp:2
	s_nop 1
	v_mfma_scale_f32_16x16x128_f8f6f4 v[42:45], v[14:19], v[218:223], v[42:45], v164, v238 op_sel_hi:[0,0,0] cbsz:2 blgp:2
	v_mov_b32_e32 v228, v240
	v_mov_b32_e32 v229, v241
	s_nop 1
	v_mfma_scale_f32_16x16x128_f8f6f4 v[38:41], v[20:25], v[224:229], v[38:41], v168, v242 op_sel_hi:[0,0,0] cbsz:2 blgp:2
	s_nop 1
	v_mfma_scale_f32_16x16x128_f8f6f4 v[26:29], v[14:19], v[224:229], v[26:29], v164, v242 op_sel_hi:[0,0,0] cbsz:2 blgp:2
	s_setprio 0
	s_setprio 1
	s_nop 1
	v_mfma_scale_f32_16x16x128_f8f6f4 v[82:85], v[8:13], v[206:211], v[82:85], v156, v230 op_sel_hi:[0,0,0] cbsz:2 blgp:2
	s_nop 1
	v_mfma_scale_f32_16x16x128_f8f6f4 v[78:81], v[2:7], v[206:211], v[78:81], v160, v230 op_sel_hi:[0,0,0] cbsz:2 blgp:2
	s_nop 1
	v_mfma_scale_f32_16x16x128_f8f6f4 v[66:69], v[8:13], v[212:217], v[66:69], v156, v234 op_sel_hi:[0,0,0] cbsz:2 blgp:2
	s_nop 1
	v_mfma_scale_f32_16x16x128_f8f6f4 v[62:65], v[2:7], v[212:217], v[62:65], v160, v234 op_sel_hi:[0,0,0] cbsz:2 blgp:2
	s_nop 1
	v_mfma_scale_f32_16x16x128_f8f6f4 v[50:53], v[8:13], v[218:223], v[50:53], v156, v238 op_sel_hi:[0,0,0] cbsz:2 blgp:2
	s_nop 1
	v_mfma_scale_f32_16x16x128_f8f6f4 v[46:49], v[2:7], v[218:223], v[46:49], v160, v238 op_sel_hi:[0,0,0] cbsz:2 blgp:2
	s_nop 1
	v_mfma_scale_f32_16x16x128_f8f6f4 v[34:37], v[8:13], v[224:229], v[34:37], v156, v242 op_sel_hi:[0,0,0] cbsz:2 blgp:2
	s_nop 1
	v_mfma_scale_f32_16x16x128_f8f6f4 v[30:33], v[2:7], v[224:229], v[30:33], v160, v242 op_sel_hi:[0,0,0] cbsz:2 blgp:2
	s_setprio 0
	s_barrier
	s_add_i32 s63, s63, 2
	s_add_u32 s20, s20, 0x100
	s_addc_u32 s21, s21, 0
	s_add_u32 s61, s61, 0x100
	s_addc_u32 s62, s62, 0
	s_cmp_gt_u32 s63, 13
	s_cbranch_scc0 .LBB0_1257
	s_and_b64 vcc, exec, s[8:9]
	s_cbranch_vccz .LBB0_1260
	s_barrier

.LBB0_1279:
	ds_read_b128 v[20:23], v195
	ds_read_b128 v[166:169], v195 offset:1024
	ds_read_b128 v[14:17], v195 offset:2048
	ds_read_b128 v[162:165], v195 offset:3072
	ds_read_b128 v[8:11], v196
	ds_read_b128 v[158:161], v196 offset:1024
	ds_read_b128 v[2:5], v196 offset:2048
	ds_read_b128 v[154:157], v196 offset:3072
	s_add_u32 s24, s22, 0xfffc0080
	s_addc_u32 s25, s23, -1
	s_cmp_eq_u32 s61, 12
	s_cselect_b32 s27, s11, s25
	s_cselect_b32 s26, s49, s24
	s_cselect_b32 s25, s13, s60
	s_cselect_b32 s24, s50, s51
	s_mov_b32 m0, s46
	ds_read_b128 v[184:187], v198
	ds_read_b128 v[188:191], v198 offset:1024
	ds_read_b128 v[202:205], v198 offset:2048
	ds_read_b128 v[218:221], v198 offset:3072
	ds_read_b128 v[208:211], v198 offset:4096
	ds_read_b128 v[222:225], v198 offset:5120
	ds_read_b128 v[214:217], v198 offset:6144
	ds_read_b128 v[226:229], v198 offset:7168
	global_load_lds_dwordx4 v180, s[22:23]
	s_add_i32 m0, s21, 0xe000
	s_nop 0
	global_load_lds_dwordx4 v182, s[22:23]
	s_waitcnt vmcnt(8)
	s_waitcnt lgkmcnt(0)
	s_barrier
	s_setprio 1
	s_waitcnt lgkmcnt(0)
	v_mov_b32_e32 v24, v166
	v_mov_b32_e32 v25, v167
	s_nop 1
	v_mfma_scale_f32_16x16x128_f8f6f4 v[150:153], v[20:25], v[184:189], v[150:153], v168, v190 op_sel_hi:[0,0,0] cbsz:2 blgp:2
	v_mov_b32_e32 v18, v162
	v_mov_b32_e32 v19, v163
	s_nop 1
	v_mfma_scale_f32_16x16x128_f8f6f4 v[138:141], v[14:19], v[184:189], v[138:141], v164, v190 op_sel_hi:[0,0,0] cbsz:2 blgp:2
	v_mov_b32_e32 v206, v218
	v_mov_b32_e32 v207, v219
	s_nop 1
	v_mfma_scale_f32_16x16x128_f8f6f4 v[134:137], v[20:25], v[202:207], v[134:137], v168, v220 op_sel_hi:[0,0,0] cbsz:2 blgp:2
	s_nop 1
	v_mfma_scale_f32_16x16x128_f8f6f4 v[122:125], v[14:19], v[202:207], v[122:125], v164, v220 op_sel_hi:[0,0,0] cbsz:2 blgp:2
	v_mov_b32_e32 v212, v222
	v_mov_b32_e32 v213, v223
	s_nop 1
	v_mfma_scale_f32_16x16x128_f8f6f4 v[118:121], v[20:25], v[208:213], v[118:121], v168, v224 op_sel_hi:[0,0,0] cbsz:2 blgp:2
	s_nop 1
	v_mfma_scale_f32_16x16x128_f8f6f4 v[106:109], v[14:19], v[208:213], v[106:109], v164, v224 op_sel_hi:[0,0,0] cbsz:2 blgp:2
	v_mov_b32_e32 v218, v226
	v_mov_b32_e32 v219, v227
	s_nop 1
	v_mfma_scale_f32_16x16x128_f8f6f4 v[102:105], v[20:25], v[214:219], v[102:105], v168, v228 op_sel_hi:[0,0,0] cbsz:2 blgp:2
	s_nop 1
	v_mfma_scale_f32_16x16x128_f8f6f4 v[90:93], v[14:19], v[214:219], v[90:93], v164, v228 op_sel_hi:[0,0,0] cbsz:2 blgp:2
	s_setprio 0
	s_setprio 1
	v_mov_b32_e32 v12, v158
	v_mov_b32_e32 v13, v159
	s_nop 1
	v_mfma_scale_f32_16x16x128_f8f6f4 v[146:149], v[8:13], v[184:189], v[146:149], v160, v190 op_sel_hi:[0,0,0] cbsz:2 blgp:2
	v_mov_b32_e32 v6, v154
	v_mov_b32_e32 v7, v155
	s_nop 1
	v_mfma_scale_f32_16x16x128_f8f6f4 v[142:145], v[2:7], v[184:189], v[142:145], v156, v190 op_sel_hi:[0,0,0] cbsz:2 blgp:2
	s_nop 1
	v_mfma_scale_f32_16x16x128_f8f6f4 v[130:133], v[8:13], v[202:207], v[130:133], v160, v220 op_sel_hi:[0,0,0] cbsz:2 blgp:2
	s_nop 1
	v_mfma_scale_f32_16x16x128_f8f6f4 v[126:129], v[2:7], v[202:207], v[126:129], v156, v220 op_sel_hi:[0,0,0] cbsz:2 blgp:2
	s_nop 1
	v_mfma_scale_f32_16x16x128_f8f6f4 v[114:117], v[8:13], v[208:213], v[114:117], v160, v224 op_sel_hi:[0,0,0] cbsz:2 blgp:2
	s_nop 1
	v_mfma_scale_f32_16x16x128_f8f6f4 v[110:113], v[2:7], v[208:213], v[110:113], v156, v224 op_sel_hi:[0,0,0] cbsz:2 blgp:2
	s_nop 1
	v_mfma_scale_f32_16x16x128_f8f6f4 v[98:101], v[8:13], v[214:219], v[98:101], v160, v228 op_sel_hi:[0,0,0] cbsz:2 blgp:2
	s_nop 1
	v_mfma_scale_f32_16x16x128_f8f6f4 v[94:97], v[2:7], v[214:219], v[94:97], v156, v228 op_sel_hi:[0,0,0] cbsz:2 blgp:2
	s_setprio 0
	s_barrier
	s_add_i32 s62, s42, s35
	s_mov_b32 m0, s62
	ds_read_b128 v[202:205], v198 offset:16384
	ds_read_b128 v[224:227], v198 offset:17408
	ds_read_b128 v[208:211], v198 offset:18432
	ds_read_b128 v[228:231], v198 offset:19456
	ds_read_b128 v[214:217], v198 offset:20480
	ds_read_b128 v[232:235], v198 offset:21504
	ds_read_b128 v[220:223], v198 offset:22528
	ds_read_b128 v[236:239], v198 offset:23552
	global_load_lds_dwordx4 v176, s[24:25]
	s_add_i32 m0, s62, 0x2000
	s_add_u32 s62, s24, 0x40000
	s_addc_u32 s63, s25, 0
	s_add_i32 s64, s43, s35
	global_load_lds_dwordx4 v172, s[24:25]
	s_mov_b32 m0, s64
	s_nop 0
	global_load_lds_dwordx4 v176, s[62:63]
	s_add_i32 m0, s64, 0x2000
	s_nop 0
	global_load_lds_dwordx4 v172, s[62:63]
	s_mov_b32 m0, s21
	s_nop 0
	global_load_lds_dwordx4 v178, s[26:27]
	s_mov_b32 m0, s36
	s_nop 0
	global_load_lds_dwordx4 v174, s[26:27]
	s_add_u32 s98, s24, 0x80
	s_addc_u32 s99, s25, 0
	s_add_u32 s100, s26, 0x80
	s_addc_u32 s101, s27, 0
	s_waitcnt vmcnt(8)
	s_waitcnt lgkmcnt(0)
	s_barrier
	s_setprio 1
	s_waitcnt lgkmcnt(0)
	v_mov_b32_e32 v206, v224
	v_mov_b32_e32 v207, v225
	s_nop 1
	v_mfma_scale_f32_16x16x128_f8f6f4 v[86:89], v[20:25], v[202:207], v[86:89], v168, v226 op_sel_hi:[0,0,0] cbsz:2 blgp:2
	s_nop 1
	v_mfma_scale_f32_16x16x128_f8f6f4 v[74:77], v[14:19], v[202:207], v[74:77], v164, v226 op_sel_hi:[0,0,0] cbsz:2 blgp:2
	v_mov_b32_e32 v212, v228
	v_mov_b32_e32 v213, v229
	s_nop 1
	v_mfma_scale_f32_16x16x128_f8f6f4 v[70:73], v[20:25], v[208:213], v[70:73], v168, v230 op_sel_hi:[0,0,0] cbsz:2 blgp:2
	s_nop 1
	v_mfma_scale_f32_16x16x128_f8f6f4 v[58:61], v[14:19], v[208:213], v[58:61], v164, v230 op_sel_hi:[0,0,0] cbsz:2 blgp:2
	v_mov_b32_e32 v218, v232
	v_mov_b32_e32 v219, v233
	s_nop 1
	v_mfma_scale_f32_16x16x128_f8f6f4 v[54:57], v[20:25], v[214:219], v[54:57], v168, v234 op_sel_hi:[0,0,0] cbsz:2 blgp:2
	s_nop 1
	v_mfma_scale_f32_16x16x128_f8f6f4 v[42:45], v[14:19], v[214:219], v[42:45], v164, v234 op_sel_hi:[0,0,0] cbsz:2 blgp:2
	v_mov_b32_e32 v224, v236
	v_mov_b32_e32 v225, v237
	s_nop 1
	v_mfma_scale_f32_16x16x128_f8f6f4 v[38:41], v[20:25], v[220:225], v[38:41], v168, v238 op_sel_hi:[0,0,0] cbsz:2 blgp:2
	s_nop 1
	v_mfma_scale_f32_16x16x128_f8f6f4 v[26:29], v[14:19], v[220:225], v[26:29], v164, v238 op_sel_hi:[0,0,0] cbsz:2 blgp:2
	s_setprio 0
	s_setprio 1
	s_nop 1
	v_mfma_scale_f32_16x16x128_f8f6f4 v[82:85], v[8:13], v[202:207], v[82:85], v160, v226 op_sel_hi:[0,0,0] cbsz:2 blgp:2
	s_nop 1
	v_mfma_scale_f32_16x16x128_f8f6f4 v[78:81], v[2:7], v[202:207], v[78:81], v156, v226 op_sel_hi:[0,0,0] cbsz:2 blgp:2
	s_nop 1
	v_mfma_scale_f32_16x16x128_f8f6f4 v[66:69], v[8:13], v[208:213], v[66:69], v160, v230 op_sel_hi:[0,0,0] cbsz:2 blgp:2
	s_nop 1
	v_mfma_scale_f32_16x16x128_f8f6f4 v[62:65], v[2:7], v[208:213], v[62:65], v156, v230 op_sel_hi:[0,0,0] cbsz:2 blgp:2
	s_nop 1
	v_mfma_scale_f32_16x16x128_f8f6f4 v[50:53], v[8:13], v[214:219], v[50:53], v160, v234 op_sel_hi:[0,0,0] cbsz:2 blgp:2
	s_nop 1
	v_mfma_scale_f32_16x16x128_f8f6f4 v[46:49], v[2:7], v[214:219], v[46:49], v156, v234 op_sel_hi:[0,0,0] cbsz:2 blgp:2
	s_nop 1
	v_mfma_scale_f32_16x16x128_f8f6f4 v[34:37], v[8:13], v[220:225], v[34:37], v160, v238 op_sel_hi:[0,0,0] cbsz:2 blgp:2
	s_nop 1
	v_mfma_scale_f32_16x16x128_f8f6f4 v[30:33], v[2:7], v[220:225], v[30:33], v156, v238 op_sel_hi:[0,0,0] cbsz:2 blgp:2
	s_setprio 0
	s_barrier
	s_add_i32 s62, 0, 0x18000
	s_add_i32 s63, 0, 0x1c000
	v_add_u32_e32 v2, s62, v194
	v_add_u32_e32 v6, s63, v194
	ds_read_b128 v[20:23], v2
	ds_read_b128 v[166:169], v2 offset:1024
	ds_read_b128 v[14:17], v2 offset:2048
	ds_read_b128 v[162:165], v2 offset:3072
	ds_read_b128 v[8:11], v6
	ds_read_b128 v[154:157], v6 offset:1024
	ds_read_b128 v[2:5], v6 offset:2048
	ds_read_b128 v[158:161], v6 offset:3072
	s_add_u32 s26, s26, 0x40000
	s_addc_u32 s27, s27, 0
	s_mov_b32 m0, s37
	ds_read_b128 v[202:205], v198 offset:32768
	ds_read_b128 v[224:227], v198 offset:33792
	ds_read_b128 v[208:211], v198 offset:34816
	ds_read_b128 v[228:231], v198 offset:35840
	ds_read_b128 v[214:217], v198 offset:36864
	ds_read_b128 v[232:235], v198 offset:37888
	ds_read_b128 v[220:223], v198 offset:38912
	ds_read_b128 v[236:239], v198 offset:39936
	global_load_lds_dwordx4 v178, s[26:27]
	s_mov_b32 m0, s38
	s_nop 0
	global_load_lds_dwordx4 v174, s[26:27]
	s_waitcnt vmcnt(8)
	s_waitcnt lgkmcnt(0)
	s_barrier
	s_setprio 1
	s_waitcnt lgkmcnt(0)
	v_mov_b32_e32 v24, v166
	v_mov_b32_e32 v25, v167
	v_mov_b32_e32 v206, v224
	v_mov_b32_e32 v207, v225
	s_nop 1
	v_mfma_scale_f32_16x16x128_f8f6f4 v[150:153], v[20:25], v[202:207], v[150:153], v168, v226 op_sel_hi:[0,0,0] cbsz:2 blgp:2
	v_mov_b32_e32 v18, v162
	v_mov_b32_e32 v19, v163
	s_nop 1
	v_mfma_scale_f32_16x16x128_f8f6f4 v[138:141], v[14:19], v[202:207], v[138:141], v164, v226 op_sel_hi:[0,0,0] cbsz:2 blgp:2
	v_mov_b32_e32 v212, v228
	v_mov_b32_e32 v213, v229
	s_nop 1
	v_mfma_scale_f32_16x16x128_f8f6f4 v[134:137], v[20:25], v[208:213], v[134:137], v168, v230 op_sel_hi:[0,0,0] cbsz:2 blgp:2
	s_nop 1
	v_mfma_scale_f32_16x16x128_f8f6f4 v[122:125], v[14:19], v[208:213], v[122:125], v164, v230 op_sel_hi:[0,0,0] cbsz:2 blgp:2
	v_mov_b32_e32 v218, v232
	v_mov_b32_e32 v219, v233
	s_nop 1
	v_mfma_scale_f32_16x16x128_f8f6f4 v[118:121], v[20:25], v[214:219], v[118:121], v168, v234 op_sel_hi:[0,0,0] cbsz:2 blgp:2
	s_nop 1
	v_mfma_scale_f32_16x16x128_f8f6f4 v[106:109], v[14:19], v[214:219], v[106:109], v164, v234 op_sel_hi:[0,0,0] cbsz:2 blgp:2
	v_mov_b32_e32 v224, v236
	v_mov_b32_e32 v225, v237
	s_nop 1
	v_mfma_scale_f32_16x16x128_f8f6f4 v[102:105], v[20:25], v[220:225], v[102:105], v168, v238 op_sel_hi:[0,0,0] cbsz:2 blgp:2
	s_nop 1
	v_mfma_scale_f32_16x16x128_f8f6f4 v[90:93], v[14:19], v[220:225], v[90:93], v164, v238 op_sel_hi:[0,0,0] cbsz:2 blgp:2
	s_setprio 0
	s_setprio 1
	v_mov_b32_e32 v12, v154
	v_mov_b32_e32 v13, v155
	s_nop 1
	v_mfma_scale_f32_16x16x128_f8f6f4 v[146:149], v[8:13], v[202:207], v[146:149], v156, v226 op_sel_hi:[0,0,0] cbsz:2 blgp:2
	v_mov_b32_e32 v6, v158
	v_mov_b32_e32 v7, v159
	s_nop 1
	v_mfma_scale_f32_16x16x128_f8f6f4 v[142:145], v[2:7], v[202:207], v[142:145], v160, v226 op_sel_hi:[0,0,0] cbsz:2 blgp:2
	s_nop 1
	v_mfma_scale_f32_16x16x128_f8f6f4 v[130:133], v[8:13], v[208:213], v[130:133], v156, v230 op_sel_hi:[0,0,0] cbsz:2 blgp:2
	s_nop 1
	v_mfma_scale_f32_16x16x128_f8f6f4 v[126:129], v[2:7], v[208:213], v[126:129], v160, v230 op_sel_hi:[0,0,0] cbsz:2 blgp:2
	s_nop 1
	v_mfma_scale_f32_16x16x128_f8f6f4 v[114:117], v[8:13], v[214:219], v[114:117], v156, v234 op_sel_hi:[0,0,0] cbsz:2 blgp:2
	s_nop 1
	v_mfma_scale_f32_16x16x128_f8f6f4 v[110:113], v[2:7], v[214:219], v[110:113], v160, v234 op_sel_hi:[0,0,0] cbsz:2 blgp:2
	s_nop 1
	v_mfma_scale_f32_16x16x128_f8f6f4 v[98:101], v[8:13], v[220:225], v[98:101], v156, v238 op_sel_hi:[0,0,0] cbsz:2 blgp:2
	s_nop 1
	v_mfma_scale_f32_16x16x128_f8f6f4 v[94:97], v[2:7], v[220:225], v[94:97], v160, v238 op_sel_hi:[0,0,0] cbsz:2 blgp:2
	s_setprio 0
	s_barrier
	s_add_i32 s26, s62, s35
	s_mov_b32 m0, s26
	ds_read_b128 v[202:205], v198 offset:49152
	ds_read_b128 v[224:227], v198 offset:50176
	ds_read_b128 v[208:211], v198 offset:51200
	ds_read_b128 v[228:231], v198 offset:52224
	ds_read_b128 v[214:217], v198 offset:53248
	ds_read_b128 v[232:235], v198 offset:54272
	ds_read_b128 v[220:223], v198 offset:55296
	ds_read_b128 v[236:239], v198 offset:56320
	global_load_lds_dwordx4 v176, s[98:99]
	s_add_i32 m0, s26, 0x2000
	s_add_u32 s24, s24, 0x40080
	s_addc_u32 s25, s25, 0
	s_add_i32 s26, s63, s35
	global_load_lds_dwordx4 v172, s[98:99]
	s_mov_b32 m0, s26
	s_nop 0
	global_load_lds_dwordx4 v176, s[24:25]
	s_add_i32 m0, s26, 0x2000
	s_nop 0
	global_load_lds_dwordx4 v172, s[24:25]
	s_mov_b32 m0, s40
	s_nop 0
	global_load_lds_dwordx4 v178, s[100:101]
	s_mov_b32 m0, s41
	s_nop 0
	global_load_lds_dwordx4 v174, s[100:101]
	s_waitcnt vmcnt(8)
	s_waitcnt lgkmcnt(0)
	s_barrier
	s_setprio 1
	s_waitcnt lgkmcnt(0)
	v_mov_b32_e32 v206, v224
	v_mov_b32_e32 v207, v225
	s_nop 1
	v_mfma_scale_f32_16x16x128_f8f6f4 v[86:89], v[20:25], v[202:207], v[86:89], v168, v226 op_sel_hi:[0,0,0] cbsz:2 blgp:2
	s_nop 1
	v_mfma_scale_f32_16x16x128_f8f6f4 v[74:77], v[14:19], v[202:207], v[74:77], v164, v226 op_sel_hi:[0,0,0] cbsz:2 blgp:2
	v_mov_b32_e32 v212, v228
	v_mov_b32_e32 v213, v229
	s_nop 1
	v_mfma_scale_f32_16x16x128_f8f6f4 v[70:73], v[20:25], v[208:213], v[70:73], v168, v230 op_sel_hi:[0,0,0] cbsz:2 blgp:2
	s_nop 1
	v_mfma_scale_f32_16x16x128_f8f6f4 v[58:61], v[14:19], v[208:213], v[58:61], v164, v230 op_sel_hi:[0,0,0] cbsz:2 blgp:2
	v_mov_b32_e32 v218, v232
	v_mov_b32_e32 v219, v233
	s_nop 1
	v_mfma_scale_f32_16x16x128_f8f6f4 v[54:57], v[20:25], v[214:219], v[54:57], v168, v234 op_sel_hi:[0,0,0] cbsz:2 blgp:2
	s_nop 1
	v_mfma_scale_f32_16x16x128_f8f6f4 v[42:45], v[14:19], v[214:219], v[42:45], v164, v234 op_sel_hi:[0,0,0] cbsz:2 blgp:2
	v_mov_b32_e32 v224, v236
	v_mov_b32_e32 v225, v237
	s_nop 1
	v_mfma_scale_f32_16x16x128_f8f6f4 v[38:41], v[20:25], v[220:225], v[38:41], v168, v238 op_sel_hi:[0,0,0] cbsz:2 blgp:2
	s_nop 1
	v_mfma_scale_f32_16x16x128_f8f6f4 v[26:29], v[14:19], v[220:225], v[26:29], v164, v238 op_sel_hi:[0,0,0] cbsz:2 blgp:2
	s_setprio 0
	s_setprio 1
	s_nop 1
	v_mfma_scale_f32_16x16x128_f8f6f4 v[82:85], v[8:13], v[202:207], v[82:85], v156, v226 op_sel_hi:[0,0,0] cbsz:2 blgp:2
	s_nop 1
	v_mfma_scale_f32_16x16x128_f8f6f4 v[78:81], v[2:7], v[202:207], v[78:81], v160, v226 op_sel_hi:[0,0,0] cbsz:2 blgp:2
	s_nop 1
	v_mfma_scale_f32_16x16x128_f8f6f4 v[66:69], v[8:13], v[208:213], v[66:69], v156, v230 op_sel_hi:[0,0,0] cbsz:2 blgp:2
	s_nop 1
	v_mfma_scale_f32_16x16x128_f8f6f4 v[62:65], v[2:7], v[208:213], v[62:65], v160, v230 op_sel_hi:[0,0,0] cbsz:2 blgp:2
	s_nop 1
	v_mfma_scale_f32_16x16x128_f8f6f4 v[50:53], v[8:13], v[214:219], v[50:53], v156, v234 op_sel_hi:[0,0,0] cbsz:2 blgp:2
	s_nop 1
	v_mfma_scale_f32_16x16x128_f8f6f4 v[46:49], v[2:7], v[214:219], v[46:49], v160, v234 op_sel_hi:[0,0,0] cbsz:2 blgp:2
	s_nop 1
	v_mfma_scale_f32_16x16x128_f8f6f4 v[34:37], v[8:13], v[220:225], v[34:37], v156, v238 op_sel_hi:[0,0,0] cbsz:2 blgp:2
	s_nop 1
	v_mfma_scale_f32_16x16x128_f8f6f4 v[30:33], v[2:7], v[220:225], v[30:33], v160, v238 op_sel_hi:[0,0,0] cbsz:2 blgp:2
	s_setprio 0
	s_barrier
	s_add_i32 s61, s61, 2
	s_add_u32 s22, s22, 0x100
	s_addc_u32 s23, s23, 0
	s_add_u32 s51, s51, 0x100
	s_addc_u32 s60, s60, 0
	s_cmp_gt_u32 s61, 13
	s_cbranch_scc0 .LBB0_1279
	s_and_b64 vcc, exec, s[8:9]
	s_cbranch_vccz .LBB0_1282
	s_barrier

.LBB0_1391:
	ds_read_b128 v[24:27], v186
	ds_read_b128 v[28:31], v186 offset:1024
	ds_read_b128 v[16:19], v186 offset:2048
	ds_read_b128 v[20:23], v186 offset:3072
	ds_read_b128 v[8:11], v187
	ds_read_b128 v[12:15], v187 offset:1024
	ds_read_b128 v[0:3], v187 offset:2048
	ds_read_b128 v[4:7], v187 offset:3072
	s_add_u32 s26, s24, 0xfff20080
	s_addc_u32 s27, s25, -1
	s_cmp_eq_u32 s67, 52
	s_cselect_b32 s29, s23, s27
	s_cselect_b32 s28, s22, s26
	s_cselect_b32 s27, s1, s66
	s_cselect_b32 s26, s0, s65
	s_add_i32 m0, s36, 0xc000
	ds_read_b128 v[174:177], v188
	ds_read_b128 v[178:181], v188 offset:1024
	ds_read_b128 v[192:195], v188 offset:2048
	ds_read_b128 v[196:199], v188 offset:3072
	ds_read_b128 v[202:205], v188 offset:4096
	ds_read_b128 v[206:209], v188 offset:5120
	ds_read_b128 v[210:213], v188 offset:6144
	ds_read_b128 v[214:217], v188 offset:7168
	global_load_lds_dwordx4 v170, s[24:25]
	s_add_i32 m0, s36, 0xe000
	s_nop 0
	global_load_lds_dwordx4 v172, s[24:25]
	s_waitcnt vmcnt(8)
	s_waitcnt lgkmcnt(0)
	s_barrier
	s_setprio 1
	s_waitcnt lgkmcnt(0)
	v_mfma_scale_f32_16x16x128_f8f6f4 v[156:159], v[24:31], v[174:181], v[156:159], v189, v190 op_sel_hi:[0,0,0]
	v_mfma_scale_f32_16x16x128_f8f6f4 v[152:155], v[16:23], v[174:181], v[152:155], v189, v190 op_sel_hi:[0,0,0]
	v_mfma_scale_f32_16x16x128_f8f6f4 v[140:143], v[24:31], v[192:199], v[140:143], v189, v190 op_sel_hi:[0,0,0]
	v_mfma_scale_f32_16x16x128_f8f6f4 v[136:139], v[16:23], v[192:199], v[136:139], v189, v190 op_sel_hi:[0,0,0]
	v_mfma_scale_f32_16x16x128_f8f6f4 v[124:127], v[24:31], v[202:209], v[124:127], v189, v190 op_sel_hi:[0,0,0]
	v_mfma_scale_f32_16x16x128_f8f6f4 v[120:123], v[16:23], v[202:209], v[120:123], v189, v190 op_sel_hi:[0,0,0]
	v_mfma_scale_f32_16x16x128_f8f6f4 v[108:111], v[24:31], v[210:217], v[108:111], v189, v190 op_sel_hi:[0,0,0]
	v_mfma_scale_f32_16x16x128_f8f6f4 v[104:107], v[16:23], v[210:217], v[104:107], v189, v190 op_sel_hi:[0,0,0]
	s_setprio 0
	s_setprio 1
	v_mfma_scale_f32_16x16x128_f8f6f4 v[148:151], v[8:15], v[174:181], v[148:151], v189, v190 op_sel_hi:[0,0,0]
	v_mfma_scale_f32_16x16x128_f8f6f4 v[144:147], v[0:7], v[174:181], v[144:147], v189, v190 op_sel_hi:[0,0,0]
	v_mfma_scale_f32_16x16x128_f8f6f4 v[132:135], v[8:15], v[192:199], v[132:135], v189, v190 op_sel_hi:[0,0,0]
	v_mfma_scale_f32_16x16x128_f8f6f4 v[128:131], v[0:7], v[192:199], v[128:131], v189, v190 op_sel_hi:[0,0,0]
	v_mfma_scale_f32_16x16x128_f8f6f4 v[116:119], v[8:15], v[202:209], v[116:119], v189, v190 op_sel_hi:[0,0,0]
	v_mfma_scale_f32_16x16x128_f8f6f4 v[112:115], v[0:7], v[202:209], v[112:115], v189, v190 op_sel_hi:[0,0,0]
	v_mfma_scale_f32_16x16x128_f8f6f4 v[100:103], v[8:15], v[210:217], v[100:103], v189, v190 op_sel_hi:[0,0,0]
	v_mfma_scale_f32_16x16x128_f8f6f4 v[96:99], v[0:7], v[210:217], v[96:99], v189, v190 op_sel_hi:[0,0,0]
	s_setprio 0
	s_barrier
	s_add_i32 s68, s44, s35
	s_mov_b32 m0, s68
	ds_read_b128 v[192:195], v188 offset:16384
	ds_read_b128 v[196:199], v188 offset:17408
	ds_read_b128 v[202:205], v188 offset:18432
	ds_read_b128 v[206:209], v188 offset:19456
	ds_read_b128 v[210:213], v188 offset:20480
	ds_read_b128 v[214:217], v188 offset:21504
	ds_read_b128 v[218:221], v188 offset:22528
	ds_read_b128 v[222:225], v188 offset:23552
	global_load_lds_dwordx4 v160, s[26:27]
	s_add_i32 m0, s68, 0x2000
	s_add_u32 s68, s26, 0xe0000
	s_addc_u32 s69, s27, 0
	s_add_i32 s70, s45, s35
	global_load_lds_dwordx4 v164, s[26:27]
	s_mov_b32 m0, s70
	s_nop 0
	global_load_lds_dwordx4 v160, s[68:69]
	s_add_i32 m0, s70, 0x2000
	s_nop 0
	global_load_lds_dwordx4 v164, s[68:69]
	s_mov_b32 m0, s36
	s_nop 0
	global_load_lds_dwordx4 v168, s[28:29]
	s_mov_b32 m0, s37
	s_nop 0
	global_load_lds_dwordx4 v166, s[28:29]
	s_add_u32 s98, s26, 0x80
	s_addc_u32 s99, s27, 0
	s_add_u32 s100, s28, 0x80
	s_addc_u32 s101, s29, 0
	s_waitcnt vmcnt(8)
	s_waitcnt lgkmcnt(0)
	s_barrier
	s_setprio 1
	s_waitcnt lgkmcnt(0)
	v_mfma_scale_f32_16x16x128_f8f6f4 v[92:95], v[24:31], v[192:199], v[92:95], v189, v190 op_sel_hi:[0,0,0]
	v_mfma_scale_f32_16x16x128_f8f6f4 v[88:91], v[16:23], v[192:199], v[88:91], v189, v190 op_sel_hi:[0,0,0]
	v_mfma_scale_f32_16x16x128_f8f6f4 v[76:79], v[24:31], v[202:209], v[76:79], v189, v190 op_sel_hi:[0,0,0]
	v_mfma_scale_f32_16x16x128_f8f6f4 v[72:75], v[16:23], v[202:209], v[72:75], v189, v190 op_sel_hi:[0,0,0]
	v_mfma_scale_f32_16x16x128_f8f6f4 v[60:63], v[24:31], v[210:217], v[60:63], v189, v190 op_sel_hi:[0,0,0]
	v_mfma_scale_f32_16x16x128_f8f6f4 v[56:59], v[16:23], v[210:217], v[56:59], v189, v190 op_sel_hi:[0,0,0]
	v_mfma_scale_f32_16x16x128_f8f6f4 v[44:47], v[24:31], v[218:225], v[44:47], v189, v190 op_sel_hi:[0,0,0]
	v_mfma_scale_f32_16x16x128_f8f6f4 v[40:43], v[16:23], v[218:225], v[40:43], v189, v190 op_sel_hi:[0,0,0]
	s_setprio 0
	s_setprio 1
	v_mfma_scale_f32_16x16x128_f8f6f4 v[84:87], v[8:15], v[192:199], v[84:87], v189, v190 op_sel_hi:[0,0,0]
	v_mfma_scale_f32_16x16x128_f8f6f4 v[80:83], v[0:7], v[192:199], v[80:83], v189, v190 op_sel_hi:[0,0,0]
	v_mfma_scale_f32_16x16x128_f8f6f4 v[68:71], v[8:15], v[202:209], v[68:71], v189, v190 op_sel_hi:[0,0,0]
	v_mfma_scale_f32_16x16x128_f8f6f4 v[64:67], v[0:7], v[202:209], v[64:67], v189, v190 op_sel_hi:[0,0,0]
	v_mfma_scale_f32_16x16x128_f8f6f4 v[52:55], v[8:15], v[210:217], v[52:55], v189, v190 op_sel_hi:[0,0,0]
	v_mfma_scale_f32_16x16x128_f8f6f4 v[48:51], v[0:7], v[210:217], v[48:51], v189, v190 op_sel_hi:[0,0,0]
	v_mfma_scale_f32_16x16x128_f8f6f4 v[36:39], v[8:15], v[218:225], v[36:39], v189, v190 op_sel_hi:[0,0,0]
	v_mfma_scale_f32_16x16x128_f8f6f4 v[32:35], v[0:7], v[218:225], v[32:35], v189, v190 op_sel_hi:[0,0,0]
	s_setprio 0
	s_barrier
	s_add_i32 s68, 0, 0x18000
	s_add_i32 s69, 0, 0x1c000
	v_add_u32_e32 v12, s68, v184
	v_add_u32_e32 v28, s69, v184
	ds_read_b128 v[0:3], v12
	ds_read_b128 v[4:7], v12 offset:1024
	ds_read_b128 v[8:11], v12 offset:2048
	ds_read_b128 v[12:15], v12 offset:3072
	ds_read_b128 v[16:19], v28
	ds_read_b128 v[20:23], v28 offset:1024
	ds_read_b128 v[24:27], v28 offset:2048
	ds_read_b128 v[28:31], v28 offset:3072
	s_add_u32 s28, s28, 0xe0000
	s_addc_u32 s29, s29, 0
	s_mov_b32 m0, s38
	ds_read_b128 v[192:195], v188 offset:32768
	ds_read_b128 v[196:199], v188 offset:33792
	ds_read_b128 v[202:205], v188 offset:34816
	ds_read_b128 v[206:209], v188 offset:35840
	ds_read_b128 v[210:213], v188 offset:36864
	ds_read_b128 v[214:217], v188 offset:37888
	ds_read_b128 v[218:221], v188 offset:38912
	ds_read_b128 v[222:225], v188 offset:39936
	global_load_lds_dwordx4 v168, s[28:29]
	s_mov_b32 m0, s39
	s_nop 0
	global_load_lds_dwordx4 v166, s[28:29]
	s_waitcnt vmcnt(8)
	s_waitcnt lgkmcnt(0)
	s_barrier
	s_setprio 1
	s_waitcnt lgkmcnt(0)
	v_mfma_scale_f32_16x16x128_f8f6f4 v[156:159], v[0:7], v[192:199], v[156:159], v189, v190 op_sel_hi:[0,0,0]
	v_mfma_scale_f32_16x16x128_f8f6f4 v[152:155], v[8:15], v[192:199], v[152:155], v189, v190 op_sel_hi:[0,0,0]
	v_mfma_scale_f32_16x16x128_f8f6f4 v[140:143], v[0:7], v[202:209], v[140:143], v189, v190 op_sel_hi:[0,0,0]
	v_mfma_scale_f32_16x16x128_f8f6f4 v[136:139], v[8:15], v[202:209], v[136:139], v189, v190 op_sel_hi:[0,0,0]
	v_mfma_scale_f32_16x16x128_f8f6f4 v[124:127], v[0:7], v[210:217], v[124:127], v189, v190 op_sel_hi:[0,0,0]
	v_mfma_scale_f32_16x16x128_f8f6f4 v[120:123], v[8:15], v[210:217], v[120:123], v189, v190 op_sel_hi:[0,0,0]
	v_mfma_scale_f32_16x16x128_f8f6f4 v[108:111], v[0:7], v[218:225], v[108:111], v189, v190 op_sel_hi:[0,0,0]
	v_mfma_scale_f32_16x16x128_f8f6f4 v[104:107], v[8:15], v[218:225], v[104:107], v189, v190 op_sel_hi:[0,0,0]
	s_setprio 0
	s_setprio 1
	v_mfma_scale_f32_16x16x128_f8f6f4 v[148:151], v[16:23], v[192:199], v[148:151], v189, v190 op_sel_hi:[0,0,0]
	v_mfma_scale_f32_16x16x128_f8f6f4 v[144:147], v[24:31], v[192:199], v[144:147], v189, v190 op_sel_hi:[0,0,0]
	v_mfma_scale_f32_16x16x128_f8f6f4 v[132:135], v[16:23], v[202:209], v[132:135], v189, v190 op_sel_hi:[0,0,0]
	v_mfma_scale_f32_16x16x128_f8f6f4 v[128:131], v[24:31], v[202:209], v[128:131], v189, v190 op_sel_hi:[0,0,0]
	v_mfma_scale_f32_16x16x128_f8f6f4 v[116:119], v[16:23], v[210:217], v[116:119], v189, v190 op_sel_hi:[0,0,0]
	v_mfma_scale_f32_16x16x128_f8f6f4 v[112:115], v[24:31], v[210:217], v[112:115], v189, v190 op_sel_hi:[0,0,0]
	v_mfma_scale_f32_16x16x128_f8f6f4 v[100:103], v[16:23], v[218:225], v[100:103], v189, v190 op_sel_hi:[0,0,0]
	v_mfma_scale_f32_16x16x128_f8f6f4 v[96:99], v[24:31], v[218:225], v[96:99], v189, v190 op_sel_hi:[0,0,0]
	s_setprio 0
	s_barrier
	s_add_i32 s28, s68, s35
	s_mov_b32 m0, s28
	ds_read_b128 v[192:195], v188 offset:49152
	ds_read_b128 v[196:199], v188 offset:50176
	ds_read_b128 v[202:205], v188 offset:51200
	ds_read_b128 v[206:209], v188 offset:52224
	ds_read_b128 v[210:213], v188 offset:53248
	ds_read_b128 v[214:217], v188 offset:54272
	ds_read_b128 v[218:221], v188 offset:55296
	ds_read_b128 v[222:225], v188 offset:56320
	global_load_lds_dwordx4 v160, s[98:99]
	s_add_i32 m0, s28, 0x2000
	s_add_u32 s26, s26, 0xe0080
	s_addc_u32 s27, s27, 0
	s_add_i32 s28, s69, s35
	global_load_lds_dwordx4 v164, s[98:99]
	s_mov_b32 m0, s28
	s_nop 0
	global_load_lds_dwordx4 v160, s[26:27]
	s_add_i32 m0, s28, 0x2000
	s_nop 0
	global_load_lds_dwordx4 v164, s[26:27]
	s_mov_b32 m0, s41
	s_nop 0
	global_load_lds_dwordx4 v168, s[100:101]
	s_mov_b32 m0, s42
	s_nop 0
	global_load_lds_dwordx4 v166, s[100:101]
	s_waitcnt vmcnt(8)
	s_waitcnt lgkmcnt(0)
	s_barrier
	s_setprio 1
	s_waitcnt lgkmcnt(0)
	v_mfma_scale_f32_16x16x128_f8f6f4 v[92:95], v[0:7], v[192:199], v[92:95], v189, v190 op_sel_hi:[0,0,0]
	v_mfma_scale_f32_16x16x128_f8f6f4 v[88:91], v[8:15], v[192:199], v[88:91], v189, v190 op_sel_hi:[0,0,0]
	v_mfma_scale_f32_16x16x128_f8f6f4 v[76:79], v[0:7], v[202:209], v[76:79], v189, v190 op_sel_hi:[0,0,0]
	v_mfma_scale_f32_16x16x128_f8f6f4 v[72:75], v[8:15], v[202:209], v[72:75], v189, v190 op_sel_hi:[0,0,0]
	v_mfma_scale_f32_16x16x128_f8f6f4 v[60:63], v[0:7], v[210:217], v[60:63], v189, v190 op_sel_hi:[0,0,0]
	v_mfma_scale_f32_16x16x128_f8f6f4 v[56:59], v[8:15], v[210:217], v[56:59], v189, v190 op_sel_hi:[0,0,0]
	v_mfma_scale_f32_16x16x128_f8f6f4 v[44:47], v[0:7], v[218:225], v[44:47], v189, v190 op_sel_hi:[0,0,0]
	v_mfma_scale_f32_16x16x128_f8f6f4 v[40:43], v[8:15], v[218:225], v[40:43], v189, v190 op_sel_hi:[0,0,0]
	s_setprio 0
	s_setprio 1
	v_mfma_scale_f32_16x16x128_f8f6f4 v[84:87], v[16:23], v[192:199], v[84:87], v189, v190 op_sel_hi:[0,0,0]
	v_mfma_scale_f32_16x16x128_f8f6f4 v[80:83], v[24:31], v[192:199], v[80:83], v189, v190 op_sel_hi:[0,0,0]
	v_mfma_scale_f32_16x16x128_f8f6f4 v[68:71], v[16:23], v[202:209], v[68:71], v189, v190 op_sel_hi:[0,0,0]
	v_mfma_scale_f32_16x16x128_f8f6f4 v[64:67], v[24:31], v[202:209], v[64:67], v189, v190 op_sel_hi:[0,0,0]
	v_mfma_scale_f32_16x16x128_f8f6f4 v[52:55], v[16:23], v[210:217], v[52:55], v189, v190 op_sel_hi:[0,0,0]
	v_mfma_scale_f32_16x16x128_f8f6f4 v[48:51], v[24:31], v[210:217], v[48:51], v189, v190 op_sel_hi:[0,0,0]
	v_mfma_scale_f32_16x16x128_f8f6f4 v[36:39], v[16:23], v[218:225], v[36:39], v189, v190 op_sel_hi:[0,0,0]
	v_mfma_scale_f32_16x16x128_f8f6f4 v[32:35], v[24:31], v[218:225], v[32:35], v189, v190 op_sel_hi:[0,0,0]
	s_setprio 0
	s_barrier
	s_add_i32 s67, s67, 2
	s_add_u32 s24, s24, 0x100
	s_addc_u32 s25, s25, 0
	s_add_u32 s65, s65, 0x100
	s_addc_u32 s66, s66, 0
	s_cmp_gt_u32 s67, 53
	s_cbranch_scc0 .LBB0_1391
	s_and_b64 vcc, exec, s[10:11]
	s_cbranch_vccz .LBB0_1394
	s_barrier
